# P6 router logits: ds_read_b128 chain software-pipelined 6 deep (counted lgkmcnt) on top of hoisted modulation loads
# speedup vs baseline: 1.0135x; 1.0054x over previous
.LBB0_2123:
	v_lshl_add_u64 v[28:29], s[44:45], 0, v[16:17]
	v_add_co_u32_e32 v4, vcc, 0x37a00000, v28
	s_add_i32 s0, s80, s8
	s_nop 0
	v_addc_co_u32_e32 v5, vcc, 0, v29, vcc
	global_load_dwordx2 v[62:63], v[4:5], off
	global_load_dwordx2 v[60:61], v[4:5], off offset:512
	global_load_dwordx2 v[48:49], v[4:5], off offset:1024
	s_waitcnt lgkmcnt(0)
	global_load_dwordx2 v[6:7], v[4:5], off offset:1536
	global_load_dwordx2 v[46:47], v[4:5], off offset:2048
	global_load_dwordx2 v[44:45], v[4:5], off offset:2560
	global_load_dwordx2 v[42:43], v[4:5], off offset:3072
	s_nop 0
	global_load_dwordx2 v[4:5], v[4:5], off offset:3584
	s_cmp_lt_i32 s0, s86
	s_cselect_b32 s48, s0, s8
	s_ashr_i32 s49, s48, 31
	s_lshl_b64 s[50:51], s[48:49], 12
	v_mov_b32_e32 v2, s81
	s_min_i32 s0, s8, 0x4000
	s_lshr_b32 s0, s0, 12
	s_mulk_i32 s0, 0x3000
	s_ashr_i32 s1, s0, 31
	s_lshl_b64 s[0:1], s[0:1], 2
	s_add_u32 s2, s6, s0
	s_addc_u32 s3, s7, s1
	s_min_i32 s0, s48, 0x4000
	s_lshr_b32 s0, s0, 12
	s_mulk_i32 s0, 0x3000
	s_ashr_i32 s1, s0, 31
	s_lshl_b64 s[0:1], s[0:1], 2
	s_add_u32 s0, s6, s0
	s_addc_u32 s1, s7, s1
	s_waitcnt vmcnt(7)
	v_and_b32_e32 v103, 0xffff0000, v63
	v_and_b32_e32 v101, 0xffff0000, v62
	v_lshlrev_b32_e32 v102, 16, v63
	s_waitcnt vmcnt(4)
	v_lshlrev_b32_e32 v25, 16, v6
	s_waitcnt vmcnt(0)
	v_lshlrev_b32_e32 v21, 16, v4
	v_and_b32_e32 v19, 0xffff0000, v4
	v_lshlrev_b32_e32 v58, 16, v5
	v_and_b32_e32 v59, 0xffff0000, v5
	v_lshl_add_u64 v[4:5], v[8:9], 0, s[50:51]
	v_and_b32_e32 v23, 0xffff0000, v6
	v_lshlrev_b32_e32 v26, 16, v7
	v_and_b32_e32 v27, 0xffff0000, v7
	global_load_dwordx2 v[40:41], v[4:5], off
	global_load_dwordx2 v[38:39], v[4:5], off offset:512
	global_load_dwordx2 v[36:37], v[4:5], off offset:1024
	global_load_dwordx2 v[6:7], v[4:5], off offset:1536
	global_load_dwordx2 v[34:35], v[4:5], off offset:2048
	global_load_dwordx2 v[32:33], v[4:5], off offset:2560
	global_load_dwordx2 v[30:31], v[4:5], off offset:3072
	global_load_dwordx2 v[50:51], v[4:5], off offset:3584
	ds_read_b64 v[64:65], v2
	v_mul_f32_e32 v2, v103, v103
	v_lshlrev_b32_e32 v100, 16, v62
	v_pk_fma_f32 v[62:63], v[102:103], v[102:103], v[2:3] op_sel_hi:[1,1,0]
	v_and_b32_e32 v99, 0xffff0000, v61
	v_and_b32_e32 v98, 0xffff0000, v60
	v_mul_f32_e32 v2, v101, v101
	v_lshlrev_b32_e32 v95, 16, v61
	v_lshlrev_b32_e32 v94, 16, v60
	v_pk_mul_f32 v[60:61], v[98:99], v[98:99]
	v_lshlrev_b32_e32 v90, 16, v48
	v_and_b32_e32 v91, 0xffff0000, v48
	v_lshlrev_b32_e32 v96, 16, v49
	v_and_b32_e32 v97, 0xffff0000, v49
	v_pk_fma_f32 v[48:49], v[100:101], v[100:101], v[2:3] op_sel_hi:[1,1,0]
	s_waitcnt lgkmcnt(0)
	v_readfirstlane_b32 s9, v64
	v_readfirstlane_b32 s12, v65
	v_pk_fma_f32 v[60:61], v[94:95], v[94:95], v[60:61]
	v_mov_b32_e32 v24, v48
	v_mov_b32_e32 v64, v62
	v_mov_b32_e32 v65, v25
	v_mul_f32_e32 v4, v23, v23
	v_pk_add_f32 v[48:49], v[48:49], v[62:63]
	v_pk_mul_f32 v[62:63], v[24:25], v[64:65]
	v_pk_add_f32 v[60:61], v[60:61], v[60:61] op_sel:[0,1] op_sel_hi:[1,0]
	v_mov_b32_e32 v49, v63
	v_mov_b32_e32 v61, v4
	v_mul_f32_e32 v2, v91, v91
	v_pk_add_f32 v[48:49], v[48:49], v[60:61]
	v_pk_fma_f32 v[60:61], v[90:91], v[90:91], v[2:3] op_sel_hi:[1,1,0]
	v_mul_f32_e32 v2, v97, v97
	v_mul_f32_e32 v18, v27, v27
	v_pk_fma_f32 v[62:63], v[96:97], v[96:97], v[2:3] op_sel_hi:[1,1,0]
	v_and_b32_e32 v107, 0xffff0000, v47
	v_mov_b32_e32 v63, v18
	v_and_b32_e32 v106, 0xffff0000, v46
	v_lshlrev_b32_e32 v105, 16, v47
	v_lshlrev_b32_e32 v104, 16, v46
	v_pk_mul_f32 v[46:47], v[106:107], v[106:107]
	v_and_b32_e32 v93, 0xffff0000, v45
	v_pk_fma_f32 v[46:47], v[104:105], v[104:105], v[46:47]
	v_and_b32_e32 v92, 0xffff0000, v44
	v_pk_add_f32 v[46:47], v[46:47], v[46:47] op_sel:[0,1] op_sel_hi:[1,0]
	v_lshlrev_b32_e32 v89, 16, v45
	v_lshlrev_b32_e32 v88, 16, v44
	v_pk_mul_f32 v[44:45], v[92:93], v[92:93]
	v_lshlrev_b32_e32 v78, 16, v42
	v_and_b32_e32 v79, 0xffff0000, v42
	v_lshlrev_b32_e32 v80, 16, v43
	v_and_b32_e32 v81, 0xffff0000, v43
	v_pk_fma_f32 v[44:45], v[88:89], v[88:89], v[44:45]
	v_mul_f32_e32 v2, v19, v19
	v_pk_add_f32 v[44:45], v[44:45], v[44:45] op_sel:[0,1] op_sel_hi:[1,0]
	s_add_u32 s52, s9, s46
	v_mov_b32_e32 v45, v2
	v_mul_f32_e32 v2, v79, v79
	s_addc_u32 s53, s12, s47
	s_add_u32 s58, s2, 0x6000
	v_mul_f32_e32 v4, v58, v58
	s_addc_u32 s59, s3, 0
	s_add_u32 s60, s2, 0x8000
	s_addc_u32 s61, s3, 0
	s_add_u32 s54, s0, 0x6000
	s_addc_u32 s55, s1, 0
	s_add_u32 s56, s0, 0x8000
	s_mov_b32 s0, 0x3a000000
	s_addc_u32 s57, s1, 0
	v_mov_b32_e32 v22, v25
	s_waitcnt vmcnt(7)
	v_and_b32_e32 v73, 0xffff0000, v41
	v_and_b32_e32 v71, 0xffff0000, v40
	v_lshlrev_b32_e32 v72, 16, v41
	s_waitcnt vmcnt(4)
	v_lshlrev_b32_e32 v55, 16, v6
	v_and_b32_e32 v53, 0xffff0000, v6
	v_mul_f32_e32 v6, v26, v26
	v_mov_b32_e32 v61, v6
	v_pk_add_f32 v[60:61], v[60:61], v[62:63]
	v_mul_f32_e32 v6, v59, v59
	v_pk_add_f32 v[48:49], v[48:49], v[60:61]
	v_lshlrev_b32_e32 v70, 16, v40
	v_pk_add_f32 v[42:43], v[48:49], v[48:49] op_sel:[0,1] op_sel_hi:[1,0]
	v_mov_b32_e32 v48, v46
	v_mov_b32_e32 v20, v42
	v_mov_b32_e32 v49, v21
	v_pk_add_f32 v[42:43], v[42:43], v[46:47]
	v_pk_mul_f32 v[46:47], v[20:21], v[48:49]
	v_and_b32_e32 v77, 0xffff0000, v39
	v_mov_b32_e32 v43, v47
	v_pk_add_f32 v[42:43], v[42:43], v[44:45]
	v_pk_fma_f32 v[44:45], v[78:79], v[78:79], v[2:3] op_sel_hi:[1,1,0]
	v_mul_f32_e32 v2, v81, v81
	v_pk_fma_f32 v[46:47], v[80:81], v[80:81], v[2:3] op_sel_hi:[1,1,0]
	v_mov_b32_e32 v45, v4
	v_mov_b32_e32 v47, v6
	v_pk_add_f32 v[44:45], v[44:45], v[46:47]
	v_mul_f32_e32 v2, v73, v73
	v_pk_add_f32 v[108:109], v[42:43], v[44:45]
	global_load_dwordx4 v[118:121], v181, s[52:53]
	global_load_dwordx4 v[122:125], v181, s[60:61]
	global_load_dwordx4 v[126:129], v181, s[58:59]
	global_load_dwordx4 v[130:133], v181, s[52:53] offset:1024
	global_load_dwordx4 v[134:137], v182, s[60:61]
	global_load_dwordx4 v[138:141], v182, s[58:59]
	global_load_dwordx4 v[142:145], v181, s[52:53] offset:2048
	global_load_dwordx4 v[146:149], v183, s[60:61]
	global_load_dwordx4 v[150:153], v183, s[58:59]
	global_load_dwordx4 v[154:157], v181, s[52:53] offset:3072
	global_load_dwordx4 v[158:161], v184, s[60:61]
	global_load_dwordx4 v[162:165], v184, s[58:59]
	global_load_dwordx4 v[166:169], v185, s[52:53]
	global_load_dwordx4 v[170:173], v185, s[60:61]
	global_load_dwordx4 v[174:177], v185, s[58:59]
	global_load_dwordx4 v[214:217], v186, s[52:53]
	global_load_dwordx4 v[224:227], v186, s[60:61]
	global_load_dwordx4 v[228:231], v186, s[58:59]
	global_load_dwordx4 v[232:235], v187, s[52:53]
	global_load_dwordx4 v[236:239], v187, s[60:61]
	global_load_dwordx4 v[240:243], v187, s[58:59]
	global_load_dwordx4 v[244:247], v190, s[52:53]
	global_load_dwordx4 v[248:251], v190, s[60:61]
	v_pk_fma_f32 v[40:41], v[72:73], v[72:73], v[2:3] op_sel_hi:[1,1,0]
	v_and_b32_e32 v76, 0xffff0000, v38
	v_mul_f32_e32 v2, v71, v71
	v_lshlrev_b32_e32 v75, 16, v39
	v_lshlrev_b32_e32 v74, 16, v38
	v_pk_mul_f32 v[38:39], v[76:77], v[76:77]
	v_lshlrev_b32_e32 v62, 16, v36
	v_and_b32_e32 v63, 0xffff0000, v36
	v_lshlrev_b32_e32 v64, 16, v37
	v_and_b32_e32 v65, 0xffff0000, v37
	v_pk_fma_f32 v[36:37], v[70:71], v[70:71], v[2:3] op_sel_hi:[1,1,0]
	v_pk_fma_f32 v[38:39], v[74:75], v[74:75], v[38:39]
	v_mov_b32_e32 v54, v36
	v_mul_f32_e32 v4, v53, v53
	v_pk_add_f32 v[36:37], v[36:37], v[40:41]
	v_pk_add_f32 v[38:39], v[38:39], v[38:39] op_sel:[0,1] op_sel_hi:[1,0]
	v_mul_f32_e32 v2, v63, v63
	v_mov_b32_e32 v39, v4
	v_lshlrev_b32_e32 v56, 16, v7
	v_and_b32_e32 v57, 0xffff0000, v7
	v_mul_f32_e32 v6, v56, v56
	v_mul_f32_e32 v18, v57, v57
	s_waitcnt vmcnt(26)
	v_and_b32_e32 v69, 0xffff0000, v35
	v_and_b32_e32 v68, 0xffff0000, v34
	v_lshlrev_b32_e32 v67, 16, v35
	v_lshlrev_b32_e32 v66, 16, v34
	v_pk_mul_f32 v[34:35], v[68:69], v[68:69]
	s_waitcnt vmcnt(25)
	v_and_b32_e32 v87, 0xffff0000, v33
	v_pk_fma_f32 v[34:35], v[66:67], v[66:67], v[34:35]
	v_and_b32_e32 v86, 0xffff0000, v32
	s_waitcnt vmcnt(23)
	v_lshlrev_b32_e32 v7, 16, v50
	v_pk_add_f32 v[34:35], v[34:35], v[34:35] op_sel:[0,1] op_sel_hi:[1,0]
	v_lshlrev_b32_e32 v61, 16, v33
	v_lshlrev_b32_e32 v60, 16, v32
	v_pk_mul_f32 v[32:33], v[86:87], v[86:87]
	v_lshlrev_b32_e32 v82, 16, v30
	v_and_b32_e32 v83, 0xffff0000, v30
	v_lshlrev_b32_e32 v84, 16, v31
	v_and_b32_e32 v85, 0xffff0000, v31
	v_and_b32_e32 v5, 0xffff0000, v50
	v_pk_fma_f32 v[32:33], v[60:61], v[60:61], v[32:33]
	v_lshlrev_b32_e32 v50, 16, v51
	v_pk_add_f32 v[32:33], v[32:33], v[32:33] op_sel:[0,1] op_sel_hi:[1,0]
	v_and_b32_e32 v51, 0xffff0000, v51
	v_mul_f32_e32 v4, v50, v50
	v_mov_b32_e32 v52, v55
	s_waitcnt vmcnt(21)
	v_mov_b32_e32 v42, v118
	v_mov_b32_e32 v43, v119
	v_mov_b32_e32 v44, v120
	v_mov_b32_e32 v45, v121
	v_mov_b32_e32 v46, v122
	v_mov_b32_e32 v47, v123
	v_mov_b32_e32 v48, v124
	v_mov_b32_e32 v49, v125
	global_load_dwordx4 v[118:121], v190, s[58:59]
	global_load_dwordx4 v[122:125], v181, s[52:53]
	v_pk_add_f32 v[212:213], v[46:47], 1.0 op_sel_hi:[1,0]
	v_mov_b32_e32 v46, v40
	v_mov_b32_e32 v47, v55
	v_pk_mul_f32 v[40:41], v[54:55], v[46:47]
	v_pk_add_f32 v[48:49], v[48:49], 1.0 op_sel_hi:[1,0]
	v_mov_b32_e32 v37, v41
	v_pk_add_f32 v[36:37], v[36:37], v[38:39]
	v_pk_fma_f32 v[38:39], v[62:63], v[62:63], v[2:3] op_sel_hi:[1,1,0]
	v_mul_f32_e32 v2, v65, v65
	v_pk_fma_f32 v[40:41], v[64:65], v[64:65], v[2:3] op_sel_hi:[1,1,0]
	v_mov_b32_e32 v39, v6
	v_mov_b32_e32 v41, v18
	v_pk_add_f32 v[38:39], v[38:39], v[40:41]
	v_mul_f32_e32 v2, v5, v5
	v_pk_add_f32 v[36:37], v[36:37], v[38:39]
	v_mov_b32_e32 v33, v2
	v_pk_add_f32 v[30:31], v[36:37], v[36:37] op_sel:[0,1] op_sel_hi:[1,0]
	v_mov_b32_e32 v36, v34
	v_mov_b32_e32 v6, v30
	v_mov_b32_e32 v37, v7
	v_pk_add_f32 v[30:31], v[30:31], v[34:35]
	v_pk_mul_f32 v[34:35], v[6:7], v[36:37]
	v_mul_f32_e32 v2, v83, v83
	v_mov_b32_e32 v31, v35
	v_pk_add_f32 v[30:31], v[30:31], v[32:33]
	v_pk_fma_f32 v[32:33], v[82:83], v[82:83], v[2:3] op_sel_hi:[1,1,0]
	v_mul_f32_e32 v2, v85, v85
	v_mul_f32_e32 v18, v51, v51
	v_pk_fma_f32 v[34:35], v[84:85], v[84:85], v[2:3] op_sel_hi:[1,1,0]
	v_mov_b32_e32 v33, v4
	v_mov_b32_e32 v35, v18
	v_pk_add_f32 v[32:33], v[32:33], v[34:35]
	v_mov_b32_e32 v40, v95
	v_pk_add_f32 v[30:31], v[30:31], v[32:33]
	v_mov_b32_e32 v33, v108
	v_mov_b32_e32 v32, v30
	v_mov_b32_e32 v108, v31
	v_pk_add_f32 v[30:31], v[32:33], v[108:109]
	v_mov_b32_e32 v41, v99
	v_mov_b32_e32 v95, v98
	v_mov_b32_dpp v33, v31 quad_perm:[1,0,3,2] row_mask:0xf bank_mask:0xf bound_ctrl:1
	v_mov_b32_dpp v32, v30 quad_perm:[1,0,3,2] row_mask:0xf bank_mask:0xf bound_ctrl:1
	v_pk_add_f32 v[30:31], v[30:31], v[32:33]
	v_mov_b32_e32 v18, v21
	s_nop 0
	v_mov_b32_dpp v33, v31 quad_perm:[2,3,0,1] row_mask:0xf bank_mask:0xf bound_ctrl:1
	v_mov_b32_dpp v32, v30 quad_perm:[2,3,0,1] row_mask:0xf bank_mask:0xf bound_ctrl:1
	v_pk_add_f32 v[30:31], v[30:31], v[32:33]
	s_nop 1
	v_mov_b32_dpp v33, v31 row_half_mirror row_mask:0xf bank_mask:0xf bound_ctrl:1
	v_mov_b32_dpp v32, v30 row_half_mirror row_mask:0xf bank_mask:0xf bound_ctrl:1
	v_pk_add_f32 v[30:31], v[30:31], v[32:33]
	s_nop 1
	v_mov_b32_dpp v33, v31 row_mirror row_mask:0xf bank_mask:0xf bound_ctrl:1
	v_mov_b32_dpp v32, v30 row_mirror row_mask:0xf bank_mask:0xf bound_ctrl:1
	v_pk_add_f32 v[30:31], v[30:31], v[32:33]
	ds_bpermute_b32 v33, v111, v31
	ds_bpermute_b32 v32, v111, v30
	s_waitcnt lgkmcnt(0)
	v_pk_add_f32 v[30:31], v[30:31], v[32:33]
	ds_bpermute_b32 v33, v112, v31
	ds_bpermute_b32 v32, v112, v30
	s_waitcnt lgkmcnt(0)
	v_pk_add_f32 v[30:31], v[30:31], v[32:33]
	s_nop 0
	v_pk_fma_f32 v[108:109], v[30:31], s[0:1], v[188:189] op_sel_hi:[1,0,0]
	s_nop 0
	v_mul_f32_e32 v2, 0x4b800000, v109
	v_cmp_gt_f32_e64 s[0:1], s11, v109
	v_cmp_gt_f32_e32 vcc, s11, v108
	s_nop 0
	v_cndmask_b32_e64 v2, v109, v2, s[0:1]
	v_rsq_f32_e32 v2, v2
	s_nop 0
	v_mul_f32_e32 v4, 0x45800000, v2
	v_cndmask_b32_e64 v2, v2, v4, s[0:1]
	v_pk_mul_f32 v[30:31], v[2:3], v[102:103] op_sel_hi:[0,1]
	v_pk_mul_f32 v[32:33], v[2:3], v[100:101] op_sel_hi:[0,1]
	v_pk_mul_f32 v[32:33], v[42:43], v[32:33]
	v_pk_mul_f32 v[30:31], v[44:45], v[30:31]
	s_mov_b32 s0, 0x40200000
	s_waitcnt vmcnt(22)
	v_mov_b32_e32 v192, v126
	v_mov_b32_e32 v193, v127
	v_mov_b32_e32 v194, v128
	v_mov_b32_e32 v195, v129
	global_load_dwordx4 v[126:129], v181, s[56:57]
	v_pk_fma_f32 v[46:47], v[48:49], v[30:31], v[194:195]
	v_pk_fma_f32 v[48:49], v[212:213], v[32:33], v[192:193]
	v_add_co_u32_e64 v100, s[0:1], s0, v28
	v_cvt_pk_bf16_f32 v30, v48, v49
	v_cvt_pk_bf16_f32 v31, v46, v47
	v_addc_co_u32_e64 v101, s[0:1], 0, v29, s[0:1]
	global_store_dwordx2 v[100:101], v[30:31], off
	s_nop 0
	v_pk_mul_f32 v[40:41], v[2:3], v[40:41] op_sel_hi:[0,1]
	v_pk_mul_f32 v[42:43], v[2:3], v[94:95] op_sel_hi:[0,1]
	v_pk_mul_f32 v[90:91], v[2:3], v[90:91] op_sel_hi:[0,1]
	v_pk_mul_f32 v[26:27], v[2:3], v[26:27] op_sel_hi:[0,1]
	v_pk_mul_f32 v[22:23], v[2:3], v[22:23] op_sel_hi:[0,1]
	v_pk_mul_f32 v[80:81], v[2:3], v[80:81] op_sel_hi:[0,1]
	v_pk_mul_f32 v[78:79], v[2:3], v[78:79] op_sel_hi:[0,1]
	v_pk_mul_f32 v[58:59], v[2:3], v[58:59] op_sel_hi:[0,1]
	v_pk_mul_f32 v[18:19], v[2:3], v[18:19] op_sel_hi:[0,1]
	s_waitcnt vmcnt(23)
	v_mov_b32_e32 v28, v130
	v_mov_b32_e32 v29, v131
	v_mov_b32_e32 v30, v132
	v_mov_b32_e32 v31, v133
	global_load_dwordx4 v[130:133], v181, s[54:55]
	v_pk_mul_f32 v[28:29], v[28:29], v[42:43]
	v_pk_mul_f32 v[30:31], v[30:31], v[40:41]
	s_waitcnt vmcnt(23)
	v_mov_b32_e32 v32, v134
	v_mov_b32_e32 v33, v135
	v_mov_b32_e32 v34, v136
	v_mov_b32_e32 v35, v137
	global_load_dwordx4 v[134:137], v181, s[52:53] offset:1024
	v_pk_add_f32 v[34:35], v[34:35], 1.0 op_sel_hi:[1,0]
	v_pk_add_f32 v[32:33], v[32:33], 1.0 op_sel_hi:[1,0]
	s_waitcnt vmcnt(23)
	v_mov_b32_e32 v36, v138
	v_mov_b32_e32 v37, v139
	v_mov_b32_e32 v38, v140
	v_mov_b32_e32 v39, v141
	global_load_dwordx4 v[138:141], v182, s[56:57]
	v_pk_fma_f32 v[42:43], v[34:35], v[30:31], v[38:39]
	v_pk_fma_f32 v[44:45], v[32:33], v[28:29], v[36:37]
	v_cvt_pk_bf16_f32 v29, v42, v43
	v_cvt_pk_bf16_f32 v28, v44, v45
	global_store_dwordx2 v[100:101], v[28:29], off offset:512
	s_nop 0
	v_pk_mul_f32 v[40:41], v[2:3], v[96:97] op_sel_hi:[0,1]
	s_waitcnt vmcnt(24)
	v_mov_b32_e32 v28, v142
	v_mov_b32_e32 v29, v143
	v_mov_b32_e32 v30, v144
	v_mov_b32_e32 v31, v145
	global_load_dwordx4 v[142:145], v182, s[54:55]
	v_pk_mul_f32 v[28:29], v[28:29], v[90:91]
	v_pk_mul_f32 v[30:31], v[30:31], v[40:41]
	s_waitcnt vmcnt(24)
	v_mov_b32_e32 v32, v146
	v_mov_b32_e32 v33, v147
	v_mov_b32_e32 v34, v148
	v_mov_b32_e32 v35, v149
	global_load_dwordx4 v[146:149], v181, s[52:53] offset:2048
	v_pk_add_f32 v[34:35], v[34:35], 1.0 op_sel_hi:[1,0]
	v_pk_add_f32 v[32:33], v[32:33], 1.0 op_sel_hi:[1,0]
	s_waitcnt vmcnt(24)
	v_mov_b32_e32 v36, v150
	v_mov_b32_e32 v37, v151
	v_mov_b32_e32 v38, v152
	v_mov_b32_e32 v39, v153
	global_load_dwordx4 v[150:153], v183, s[56:57]
	v_pk_fma_f32 v[38:39], v[34:35], v[30:31], v[38:39]
	v_pk_fma_f32 v[40:41], v[32:33], v[28:29], v[36:37]
	v_cvt_pk_bf16_f32 v29, v38, v39
	v_cvt_pk_bf16_f32 v28, v40, v41
	global_store_dwordx2 v[100:101], v[28:29], off offset:1024
	s_nop 0
	v_mov_b32_e32 v90, v89
	v_mov_b32_e32 v91, v93
	v_mov_b32_e32 v89, v92
	v_pk_mul_f32 v[90:91], v[2:3], v[90:91] op_sel_hi:[0,1]
	v_pk_mul_f32 v[88:89], v[2:3], v[88:89] op_sel_hi:[0,1]
	s_waitcnt vmcnt(25)
	v_mov_b32_e32 v28, v154
	v_mov_b32_e32 v29, v155
	v_mov_b32_e32 v30, v156
	v_mov_b32_e32 v31, v157
	global_load_dwordx4 v[154:157], v183, s[54:55]
	v_pk_mul_f32 v[22:23], v[22:23], v[28:29]
	v_pk_mul_f32 v[24:25], v[26:27], v[30:31]
	s_waitcnt vmcnt(25)
	v_mov_b32_e32 v32, v158
	v_mov_b32_e32 v33, v159
	v_mov_b32_e32 v34, v160
	v_mov_b32_e32 v35, v161
	global_load_dwordx4 v[158:161], v181, s[52:53] offset:3072
	v_pk_add_f32 v[26:27], v[34:35], 1.0 op_sel_hi:[1,0]
	v_pk_add_f32 v[28:29], v[32:33], 1.0 op_sel_hi:[1,0]
	s_waitcnt vmcnt(25)
	v_mov_b32_e32 v94, v162
	v_mov_b32_e32 v95, v163
	v_mov_b32_e32 v96, v164
	v_mov_b32_e32 v97, v165
	global_load_dwordx4 v[162:165], v184, s[56:57]
	v_pk_fma_f32 v[30:31], v[24:25], v[26:27], v[96:97]
	v_pk_fma_f32 v[32:33], v[22:23], v[28:29], v[94:95]
	v_cvt_pk_bf16_f32 v23, v30, v31
	v_cvt_pk_bf16_f32 v22, v32, v33
	global_store_dwordx2 v[100:101], v[22:23], off offset:1536
	s_nop 0
	v_mov_b32_e32 v34, v105
	v_mov_b32_e32 v35, v107
	v_mov_b32_e32 v105, v106
	v_pk_mul_f32 v[34:35], v[2:3], v[34:35] op_sel_hi:[0,1]
	v_pk_mul_f32 v[36:37], v[2:3], v[104:105] op_sel_hi:[0,1]
	v_mul_f32_e32 v2, 0x4b800000, v108
	v_cndmask_b32_e32 v2, v108, v2, vcc
	v_rsq_f32_e32 v2, v2
	s_waitcnt vmcnt(26)
	v_mov_b32_e32 v22, v166
	v_mov_b32_e32 v23, v167
	v_mov_b32_e32 v24, v168
	v_mov_b32_e32 v25, v169
	global_load_dwordx4 v[166:169], v184, s[54:55]
	v_pk_mul_f32 v[22:23], v[36:37], v[22:23]
	v_pk_mul_f32 v[24:25], v[34:35], v[24:25]
	s_waitcnt vmcnt(26)
	v_mov_b32_e32 v26, v170
	v_mov_b32_e32 v27, v171
	v_mov_b32_e32 v28, v172
	v_mov_b32_e32 v29, v173
	global_load_dwordx4 v[170:173], v185, s[52:53]
	v_pk_add_f32 v[28:29], v[28:29], 1.0 op_sel_hi:[1,0]
	v_pk_add_f32 v[26:27], v[26:27], 1.0 op_sel_hi:[1,0]
	s_waitcnt vmcnt(26)
	v_mov_b32_e32 v94, v174
	v_mov_b32_e32 v95, v175
	v_mov_b32_e32 v96, v176
	v_mov_b32_e32 v97, v177
	global_load_dwordx4 v[174:177], v185, s[56:57]
	v_pk_fma_f32 v[34:35], v[24:25], v[28:29], v[96:97]
	v_pk_fma_f32 v[36:37], v[22:23], v[26:27], v[94:95]
	v_cvt_pk_bf16_f32 v23, v34, v35
	v_cvt_pk_bf16_f32 v22, v36, v37
	global_store_dwordx2 v[100:101], v[22:23], off offset:2048
	s_nop 0
	v_mul_f32_e32 v4, 0x45800000, v2
	v_cndmask_b32_e32 v2, v2, v4, vcc
	v_pk_mul_f32 v[70:71], v[2:3], v[70:71] op_sel_hi:[0,1]
	v_pk_mul_f32 v[62:63], v[2:3], v[62:63] op_sel_hi:[0,1]
	v_pk_mul_f32 v[56:57], v[2:3], v[56:57] op_sel_hi:[0,1]
	v_pk_mul_f32 v[52:53], v[2:3], v[52:53] op_sel_hi:[0,1]
	v_pk_mul_f32 v[82:83], v[2:3], v[82:83] op_sel_hi:[0,1]
	v_mov_b32_e32 v4, v7
	v_pk_mul_f32 v[50:51], v[2:3], v[50:51] op_sel_hi:[0,1]
	v_pk_mul_f32 v[4:5], v[2:3], v[4:5] op_sel_hi:[0,1]
	s_waitcnt vmcnt(27)
	v_mov_b32_e32 v22, v214
	v_mov_b32_e32 v23, v215
	v_mov_b32_e32 v24, v216
	v_mov_b32_e32 v25, v217
	global_load_dwordx4 v[214:217], v185, s[54:55]
	v_pk_mul_f32 v[22:23], v[88:89], v[22:23]
	v_pk_mul_f32 v[24:25], v[90:91], v[24:25]
	s_waitcnt vmcnt(27)
	v_mov_b32_e32 v26, v224
	v_mov_b32_e32 v27, v225
	v_mov_b32_e32 v28, v226
	v_mov_b32_e32 v29, v227
	global_load_dwordx4 v[224:227], v186, s[52:53]
	v_pk_add_f32 v[28:29], v[28:29], 1.0 op_sel_hi:[1,0]
	v_pk_add_f32 v[88:89], v[26:27], 1.0 op_sel_hi:[1,0]
	s_waitcnt vmcnt(27)
	v_mov_b32_e32 v94, v228
	v_mov_b32_e32 v95, v229
	v_mov_b32_e32 v96, v230
	v_mov_b32_e32 v97, v231
	global_load_dwordx4 v[228:231], v186, s[56:57]
	v_pk_fma_f32 v[26:27], v[24:25], v[28:29], v[96:97]
	v_pk_fma_f32 v[28:29], v[22:23], v[88:89], v[94:95]
	v_cvt_pk_bf16_f32 v23, v26, v27
	v_cvt_pk_bf16_f32 v22, v28, v29
	global_store_dwordx2 v[100:101], v[22:23], off offset:2560
	s_nop 0
	v_lshl_add_u64 v[96:97], v[12:13], 0, s[50:51]
	s_waitcnt vmcnt(28)
	v_mov_b32_e32 v22, v232
	v_mov_b32_e32 v23, v233
	v_mov_b32_e32 v24, v234
	v_mov_b32_e32 v25, v235
	global_load_dwordx4 v[232:235], v186, s[54:55]
	v_pk_mul_f32 v[78:79], v[78:79], v[22:23]
	v_pk_mul_f32 v[22:23], v[80:81], v[24:25]
	s_waitcnt vmcnt(28)
	v_mov_b32_e32 v88, v236
	v_mov_b32_e32 v89, v237
	v_mov_b32_e32 v90, v238
	v_mov_b32_e32 v91, v239
	global_load_dwordx4 v[236:239], v187, s[52:53]
	v_pk_add_f32 v[24:25], v[90:91], 1.0 op_sel_hi:[1,0]
	v_pk_add_f32 v[80:81], v[88:89], 1.0 op_sel_hi:[1,0]
	s_waitcnt vmcnt(28)
	v_mov_b32_e32 v92, v240
	v_mov_b32_e32 v93, v241
	v_mov_b32_e32 v94, v242
	v_mov_b32_e32 v95, v243
	global_load_dwordx4 v[240:243], v187, s[56:57]
	v_pk_fma_f32 v[22:23], v[22:23], v[24:25], v[94:95]
	v_pk_fma_f32 v[24:25], v[78:79], v[80:81], v[92:93]
	v_cvt_pk_bf16_f32 v79, v22, v23
	v_cvt_pk_bf16_f32 v78, v24, v25
	global_store_dwordx2 v[100:101], v[78:79], off offset:3072
	s_nop 0
	s_waitcnt vmcnt(29)
	v_mov_b32_e32 v78, v244
	v_mov_b32_e32 v79, v245
	v_mov_b32_e32 v80, v246
	v_mov_b32_e32 v81, v247
	global_load_dwordx4 v[244:247], v187, s[54:55]
	v_pk_mul_f32 v[20:21], v[18:19], v[78:79]
	v_pk_mul_f32 v[18:19], v[58:59], v[80:81]
	s_waitcnt vmcnt(29)
	v_mov_b32_e32 v88, v248
	v_mov_b32_e32 v89, v249
	v_mov_b32_e32 v90, v250
	v_mov_b32_e32 v91, v251
	global_load_dwordx4 v[248:251], v190, s[52:53]
	v_pk_add_f32 v[58:59], v[90:91], 1.0 op_sel_hi:[1,0]
	v_pk_add_f32 v[78:79], v[88:89], 1.0 op_sel_hi:[1,0]
	s_waitcnt vmcnt(29)
	v_mov_b32_e32 v92, v118
	v_mov_b32_e32 v93, v119
	v_mov_b32_e32 v94, v120
	v_mov_b32_e32 v95, v121
	global_load_dwordx4 v[118:121], v190, s[56:57]
	v_pk_fma_f32 v[18:19], v[18:19], v[58:59], v[94:95]
	v_pk_fma_f32 v[20:21], v[20:21], v[78:79], v[92:93]
	v_cvt_pk_bf16_f32 v59, v18, v19
	v_cvt_pk_bf16_f32 v58, v20, v21
	global_store_dwordx2 v[100:101], v[58:59], off offset:3584
	v_pk_mul_f32 v[58:59], v[2:3], v[72:73] op_sel_hi:[0,1]
	s_waitcnt vmcnt(30)
	v_mov_b32_e32 v78, v122
	v_mov_b32_e32 v79, v123
	v_mov_b32_e32 v80, v124
	v_mov_b32_e32 v81, v125
	global_load_dwordx4 v[122:125], v190, s[54:55]
	v_pk_mul_f32 v[72:73], v[78:79], v[70:71]
	v_pk_mul_f32 v[58:59], v[80:81], v[58:59]
	s_waitcnt vmcnt(30)
	v_mov_b32_e32 v88, v126
	v_mov_b32_e32 v89, v127
	v_mov_b32_e32 v90, v128
	v_mov_b32_e32 v91, v129
	v_pk_add_f32 v[70:71], v[90:91], 1.0 op_sel_hi:[1,0]
	v_pk_add_f32 v[78:79], v[88:89], 1.0 op_sel_hi:[1,0]
	s_waitcnt vmcnt(28)
	v_mov_b32_e32 v92, v130
	v_mov_b32_e32 v93, v131
	v_mov_b32_e32 v94, v132
	v_mov_b32_e32 v95, v133
	v_pk_fma_f32 v[70:71], v[70:71], v[58:59], v[94:95]
	v_pk_fma_f32 v[72:73], v[78:79], v[72:73], v[92:93]
	v_cvt_pk_bf16_f32 v59, v70, v71
	v_cvt_pk_bf16_f32 v58, v72, v73
	global_store_dwordx2 v[96:97], v[58:59], off
	v_mov_b32_e32 v58, v75
	v_mov_b32_e32 v59, v77
	v_mov_b32_e32 v75, v76
	v_pk_mul_f32 v[58:59], v[2:3], v[58:59] op_sel_hi:[0,1]
	v_pk_mul_f32 v[74:75], v[2:3], v[74:75] op_sel_hi:[0,1]
	s_waitcnt vmcnt(28)
	v_mov_b32_e32 v78, v134
	v_mov_b32_e32 v79, v135
	v_mov_b32_e32 v80, v136
	v_mov_b32_e32 v81, v137
	v_pk_mul_f32 v[74:75], v[78:79], v[74:75]
	v_pk_mul_f32 v[58:59], v[80:81], v[58:59]
	s_waitcnt vmcnt(27)
	v_mov_b32_e32 v88, v138
	v_mov_b32_e32 v89, v139
	v_mov_b32_e32 v90, v140
	v_mov_b32_e32 v91, v141
	v_pk_add_f32 v[76:77], v[90:91], 1.0 op_sel_hi:[1,0]
	v_pk_add_f32 v[80:81], v[88:89], 1.0 op_sel_hi:[1,0]
	s_waitcnt vmcnt(25)
	v_mov_b32_e32 v92, v142
	v_mov_b32_e32 v93, v143
	v_mov_b32_e32 v94, v144
	v_mov_b32_e32 v95, v145
	v_pk_fma_f32 v[78:79], v[76:77], v[58:59], v[94:95]
	v_pk_fma_f32 v[80:81], v[80:81], v[74:75], v[92:93]
	v_cvt_pk_bf16_f32 v59, v78, v79
	v_cvt_pk_bf16_f32 v58, v80, v81
	global_store_dwordx2 v[96:97], v[58:59], off offset:512
	v_pk_mul_f32 v[58:59], v[2:3], v[64:65] op_sel_hi:[0,1]
	s_waitcnt vmcnt(25)
	v_mov_b32_e32 v74, v146
	v_mov_b32_e32 v75, v147
	v_mov_b32_e32 v76, v148
	v_mov_b32_e32 v77, v149
	v_pk_mul_f32 v[62:63], v[74:75], v[62:63]
	v_pk_mul_f32 v[58:59], v[76:77], v[58:59]
	s_waitcnt vmcnt(24)
	v_mov_b32_e32 v88, v150
	v_mov_b32_e32 v89, v151
	v_mov_b32_e32 v90, v152
	v_mov_b32_e32 v91, v153
	v_pk_add_f32 v[64:65], v[90:91], 1.0 op_sel_hi:[1,0]
	v_pk_add_f32 v[76:77], v[88:89], 1.0 op_sel_hi:[1,0]
	s_waitcnt vmcnt(22)
	v_mov_b32_e32 v92, v154
	v_mov_b32_e32 v93, v155
	v_mov_b32_e32 v94, v156
	v_mov_b32_e32 v95, v157
	v_pk_fma_f32 v[74:75], v[64:65], v[58:59], v[94:95]
	v_pk_fma_f32 v[76:77], v[76:77], v[62:63], v[92:93]
	v_cvt_pk_bf16_f32 v59, v74, v75
	v_cvt_pk_bf16_f32 v58, v76, v77
	global_store_dwordx2 v[96:97], v[58:59], off offset:1024
	s_waitcnt vmcnt(22)
	v_mov_b32_e32 v62, v158
	v_mov_b32_e32 v63, v159
	v_mov_b32_e32 v64, v160
	v_mov_b32_e32 v65, v161
	v_pk_mul_f32 v[52:53], v[52:53], v[62:63]
	v_pk_mul_f32 v[54:55], v[56:57], v[64:65]
	s_waitcnt vmcnt(21)
	v_mov_b32_e32 v88, v162
	v_mov_b32_e32 v89, v163
	v_mov_b32_e32 v90, v164
	v_mov_b32_e32 v91, v165
	v_pk_add_f32 v[56:57], v[90:91], 1.0 op_sel_hi:[1,0]
	v_pk_add_f32 v[58:59], v[88:89], 1.0 op_sel_hi:[1,0]
	s_waitcnt vmcnt(19)
	v_mov_b32_e32 v92, v166
	v_mov_b32_e32 v93, v167
	v_mov_b32_e32 v94, v168
	v_mov_b32_e32 v95, v169
	v_pk_fma_f32 v[62:63], v[54:55], v[56:57], v[94:95]
	v_pk_fma_f32 v[64:65], v[52:53], v[58:59], v[92:93]
	v_cvt_pk_bf16_f32 v53, v62, v63
	v_cvt_pk_bf16_f32 v52, v64, v65
	global_store_dwordx2 v[96:97], v[52:53], off offset:1536
	s_nop 0
	v_mov_b32_e32 v92, v67
	v_mov_b32_e32 v93, v69
	v_mov_b32_e32 v67, v68
	v_pk_mul_f32 v[92:93], v[2:3], v[92:93] op_sel_hi:[0,1]
	v_pk_mul_f32 v[66:67], v[2:3], v[66:67] op_sel_hi:[0,1]
	s_waitcnt vmcnt(19)
	v_mov_b32_e32 v52, v170
	v_mov_b32_e32 v53, v171
	v_mov_b32_e32 v54, v172
	v_mov_b32_e32 v55, v173
	v_pk_mul_f32 v[52:53], v[66:67], v[52:53]
	v_pk_mul_f32 v[54:55], v[92:93], v[54:55]
	s_waitcnt vmcnt(18)
	v_mov_b32_e32 v56, v174
	v_mov_b32_e32 v57, v175
	v_mov_b32_e32 v58, v176
	v_mov_b32_e32 v59, v177
	v_pk_add_f32 v[58:59], v[58:59], 1.0 op_sel_hi:[1,0]
	v_pk_add_f32 v[56:57], v[56:57], 1.0 op_sel_hi:[1,0]
	s_waitcnt vmcnt(16)
	v_mov_b32_e32 v88, v214
	v_mov_b32_e32 v89, v215
	v_mov_b32_e32 v90, v216
	v_mov_b32_e32 v91, v217
	v_pk_fma_f32 v[66:67], v[54:55], v[58:59], v[90:91]
	v_pk_fma_f32 v[68:69], v[52:53], v[56:57], v[88:89]
	v_cvt_pk_bf16_f32 v53, v66, v67
	v_cvt_pk_bf16_f32 v52, v68, v69
	global_store_dwordx2 v[96:97], v[52:53], off offset:2048
	s_nop 0
	v_mov_b32_e32 v92, v61
	v_mov_b32_e32 v93, v87
	v_mov_b32_e32 v61, v86
	v_pk_mul_f32 v[92:93], v[2:3], v[92:93] op_sel_hi:[0,1]
	v_pk_mul_f32 v[60:61], v[2:3], v[60:61] op_sel_hi:[0,1]
	s_waitcnt vmcnt(16)
	v_mov_b32_e32 v52, v224
	v_mov_b32_e32 v53, v225
	v_mov_b32_e32 v54, v226
	v_mov_b32_e32 v55, v227
	v_pk_mul_f32 v[52:53], v[60:61], v[52:53]
	v_pk_mul_f32 v[54:55], v[92:93], v[54:55]
	s_waitcnt vmcnt(15)
	v_mov_b32_e32 v56, v228
	v_mov_b32_e32 v57, v229
	v_mov_b32_e32 v58, v230
	v_mov_b32_e32 v59, v231
	v_pk_add_f32 v[58:59], v[58:59], 1.0 op_sel_hi:[1,0]
	v_pk_add_f32 v[56:57], v[56:57], 1.0 op_sel_hi:[1,0]
	s_waitcnt vmcnt(13)
	v_mov_b32_e32 v88, v232
	v_mov_b32_e32 v89, v233
	v_mov_b32_e32 v90, v234
	v_mov_b32_e32 v91, v235
	v_pk_fma_f32 v[58:59], v[54:55], v[58:59], v[90:91]
	v_pk_fma_f32 v[60:61], v[52:53], v[56:57], v[88:89]
	v_cvt_pk_bf16_f32 v53, v58, v59
	v_cvt_pk_bf16_f32 v52, v60, v61
	global_store_dwordx2 v[96:97], v[52:53], off offset:2560
	s_nop 0
	v_pk_mul_f32 v[56:57], v[2:3], v[84:85] op_sel_hi:[0,1]
	s_waitcnt vmcnt(13)
	v_mov_b32_e32 v52, v236
	v_mov_b32_e32 v53, v237
	v_mov_b32_e32 v54, v238
	v_mov_b32_e32 v55, v239
	v_pk_mul_f32 v[52:53], v[82:83], v[52:53]
	v_pk_mul_f32 v[54:55], v[56:57], v[54:55]
	s_waitcnt vmcnt(12)
	v_mov_b32_e32 v86, v240
	v_mov_b32_e32 v87, v241
	v_mov_b32_e32 v88, v242
	v_mov_b32_e32 v89, v243
	v_pk_add_f32 v[56:57], v[88:89], 1.0 op_sel_hi:[1,0]
	v_pk_add_f32 v[82:83], v[86:87], 1.0 op_sel_hi:[1,0]
	s_waitcnt vmcnt(10)
	v_mov_b32_e32 v90, v244
	v_mov_b32_e32 v91, v245
	v_mov_b32_e32 v92, v246
	v_mov_b32_e32 v93, v247
	v_pk_fma_f32 v[54:55], v[54:55], v[56:57], v[92:93]
	v_pk_fma_f32 v[56:57], v[52:53], v[82:83], v[90:91]
	v_cvt_pk_bf16_f32 v53, v54, v55
	v_cvt_pk_bf16_f32 v52, v56, v57
	global_store_dwordx2 v[96:97], v[52:53], off offset:3072
	s_waitcnt vmcnt(10)
	v_mov_b32_e32 v82, v248
	v_mov_b32_e32 v83, v249
	v_mov_b32_e32 v84, v250
	v_mov_b32_e32 v85, v251
	v_pk_mul_f32 v[4:5], v[4:5], v[82:83]
	v_pk_mul_f32 v[6:7], v[50:51], v[84:85]
	s_waitcnt vmcnt(9)
	v_mov_b32_e32 v86, v118
	v_mov_b32_e32 v87, v119
	v_mov_b32_e32 v88, v120
	v_mov_b32_e32 v89, v121
	v_pk_add_f32 v[50:51], v[88:89], 1.0 op_sel_hi:[1,0]
	v_pk_add_f32 v[52:53], v[86:87], 1.0 op_sel_hi:[1,0]
	s_waitcnt vmcnt(7)
	v_mov_b32_e32 v90, v122
	v_mov_b32_e32 v91, v123
	v_mov_b32_e32 v92, v124
	v_mov_b32_e32 v93, v125
	v_pk_fma_f32 v[50:51], v[6:7], v[50:51], v[92:93]
	v_pk_fma_f32 v[52:53], v[4:5], v[52:53], v[90:91]
	v_cvt_pk_bf16_f32 v5, v50, v51
	v_cvt_pk_bf16_f32 v4, v52, v53
	global_store_dwordx2 v[96:97], v[4:5], off offset:3584
	v_add_u32_e32 v118, 0x10400, v110
	v_add_u32_e32 v119, 0x10800, v110
	v_add_u32_e32 v120, 0x10c00, v110
	v_add_u32_e32 v121, 0x11000, v110
	v_add_u32_e32 v122, 0x11400, v110
	v_add_u32_e32 v123, 0x11800, v110
	v_add_u32_e32 v124, 0x11c00, v110
	v_add_u32_e32 v125, 0x12000, v110
	v_add_u32_e32 v126, 0x12400, v110
	v_add_u32_e32 v127, 0x12800, v110
	v_add_u32_e32 v128, 0x12c00, v110
	v_add_u32_e32 v129, 0x13000, v110
	v_add_u32_e32 v130, 0x13400, v110
	v_add_u32_e32 v131, 0x13800, v110
	v_add_u32_e32 v132, 0x13c00, v110
	v_add_u32_e32 v133, 0x14000, v110
	v_add_u32_e32 v134, 0x14400, v110
	v_add_u32_e32 v135, 0x14800, v110
	v_add_u32_e32 v136, 0x14c00, v110
	v_add_u32_e32 v137, 0x15000, v110
	v_add_u32_e32 v138, 0x15400, v110
	v_add_u32_e32 v139, 0x15800, v110
	v_add_u32_e32 v140, 0x15c00, v110
	v_add_u32_e32 v141, 0x16000, v110
	v_add_u32_e32 v142, 0x16400, v110
	v_add_u32_e32 v143, 0x16800, v110
	v_add_u32_e32 v144, 0x16c00, v110
	v_add_u32_e32 v145, 0x17000, v110
	v_add_u32_e32 v146, 0x17400, v110
	v_add_u32_e32 v147, 0x17800, v110
	v_add_u32_e32 v148, 0x17c00, v110
	v_add_u32_e32 v149, 0x18000, v110
	v_add_u32_e32 v150, 0x18400, v110
	v_add_u32_e32 v151, 0x18800, v110
	v_add_u32_e32 v152, 0x18c00, v110
	v_add_u32_e32 v153, 0x19000, v110
	v_add_u32_e32 v154, 0x19400, v110
	v_add_u32_e32 v155, 0x19800, v110
	v_add_u32_e32 v156, 0x19c00, v110
	v_add_u32_e32 v157, 0x1a000, v110
	v_add_u32_e32 v158, 0x1a400, v110
	v_add_u32_e32 v159, 0x1a800, v110
	v_add_u32_e32 v160, 0x1ac00, v110
	v_add_u32_e32 v161, 0x1b000, v110
	v_add_u32_e32 v162, 0x1b400, v110
	v_add_u32_e32 v163, 0x1b800, v110
	v_add_u32_e32 v164, 0x1bc00, v110
	v_add_u32_e32 v165, 0x1c000, v110
	v_add_u32_e32 v166, 0x1c400, v110
	v_add_u32_e32 v167, 0x1c800, v110
	v_add_u32_e32 v168, 0x1cc00, v110
	v_add_u32_e32 v169, 0x1d000, v110
	v_add_u32_e32 v170, 0x1d400, v110
	v_add_u32_e32 v171, 0x1d800, v110
	v_add_u32_e32 v172, 0x1dc00, v110
	v_add_u32_e32 v173, 0x1e000, v110
	v_add_u32_e32 v174, 0x1e400, v110
	v_add_u32_e32 v175, 0x1e800, v110
	v_add_u32_e32 v176, 0x1ec00, v110
	v_add_u32_e32 v177, 0x1f000, v110
	ds_read_b128 v[236:239], v110
	ds_read_b128 v[232:235], v110 offset:1024
	ds_read_b128 v[228:231], v110 offset:2048
	ds_read_b128 v[224:227], v110 offset:3072
	ds_read_b128 v[4:7], v110 offset:4096
	ds_read_b128 v[240:243], v110 offset:5120
	s_waitcnt lgkmcnt(5)
	v_mul_f32_e32 v2, v237, v49
	v_mul_f32_e32 v237, v237, v73
	v_fmac_f32_e32 v2, v236, v48
	v_fmac_f32_e32 v237, v236, v72
	v_mul_f32_e32 v236, v239, v71
	v_mul_f32_e32 v82, v239, v47
	v_fmac_f32_e32 v236, v238, v70
	v_fmac_f32_e32 v82, v238, v46
	v_add_f32_e32 v236, v237, v236
	v_add_f32_e32 v2, v2, v82
	v_add_f32_e32 v82, 0, v236
	ds_read_b128 v[236:239], v110 offset:6144
	v_add_f32_e32 v2, 0, v2
	s_waitcnt lgkmcnt(5)
	v_mul_f32_e32 v83, v233, v45
	v_mul_f32_e32 v233, v233, v81
	v_fmac_f32_e32 v83, v232, v44
	v_fmac_f32_e32 v233, v232, v80
	v_mul_f32_e32 v232, v235, v79
	v_fmac_f32_e32 v232, v234, v78
	v_mul_f32_e32 v84, v235, v43
	v_add_f32_e32 v232, v233, v232
	v_fmac_f32_e32 v84, v234, v42
	v_add_f32_e32 v82, v82, v232
	ds_read_b128 v[232:235], v110 offset:7168
	v_add_f32_e32 v83, v83, v84
	v_add_f32_e32 v2, v2, v83
	s_waitcnt lgkmcnt(5)
	v_mul_f32_e32 v83, v229, v41
	v_mul_f32_e32 v229, v229, v77
	v_fmac_f32_e32 v83, v228, v40
	v_fmac_f32_e32 v229, v228, v76
	v_mul_f32_e32 v228, v231, v75
	v_fmac_f32_e32 v228, v230, v74
	v_mul_f32_e32 v84, v231, v39
	v_add_f32_e32 v228, v229, v228
	v_fmac_f32_e32 v84, v230, v38
	v_add_f32_e32 v82, v82, v228
	ds_read_b128 v[228:231], v110 offset:8192
	v_add_f32_e32 v83, v83, v84
	v_add_f32_e32 v2, v2, v83
	s_waitcnt lgkmcnt(5)
	v_mul_f32_e32 v83, v225, v33
	v_mul_f32_e32 v225, v225, v65
	v_fmac_f32_e32 v83, v224, v32
	v_fmac_f32_e32 v225, v224, v64
	v_mul_f32_e32 v224, v227, v63
	v_fmac_f32_e32 v224, v226, v62
	v_mul_f32_e32 v84, v227, v31
	v_add_f32_e32 v224, v225, v224
	v_fmac_f32_e32 v84, v226, v30
	v_add_f32_e32 v82, v82, v224
	ds_read_b128 v[224:227], v110 offset:9216
	v_add_f32_e32 v83, v83, v84
	v_add_f32_e32 v2, v2, v83
	s_waitcnt lgkmcnt(5)
	v_mul_f32_e32 v83, v5, v37
	v_mul_f32_e32 v5, v5, v69
	v_fmac_f32_e32 v83, v4, v36
	v_fmac_f32_e32 v5, v4, v68
	v_mul_f32_e32 v4, v7, v67
	v_fmac_f32_e32 v4, v6, v66
	v_mul_f32_e32 v84, v7, v35
	v_add_f32_e32 v4, v5, v4
	v_fmac_f32_e32 v84, v6, v34
	v_add_f32_e32 v82, v82, v4
	ds_read_b128 v[4:7], v110 offset:10240
	v_add_f32_e32 v83, v83, v84
	v_add_f32_e32 v2, v2, v83
	s_waitcnt lgkmcnt(5)
	v_mul_f32_e32 v83, v241, v29
	v_mul_f32_e32 v241, v241, v61
	v_fmac_f32_e32 v83, v240, v28
	v_fmac_f32_e32 v241, v240, v60
	v_mul_f32_e32 v240, v243, v59
	v_fmac_f32_e32 v240, v242, v58
	v_mul_f32_e32 v84, v243, v27
	v_add_f32_e32 v240, v241, v240
	v_fmac_f32_e32 v84, v242, v26
	v_add_f32_e32 v82, v82, v240
	ds_read_b128 v[240:243], v110 offset:11264
	v_add_f32_e32 v83, v83, v84
	v_add_f32_e32 v2, v2, v83
	s_waitcnt lgkmcnt(5)
	v_mul_f32_e32 v83, v237, v25
	v_mul_f32_e32 v237, v237, v57
	v_fmac_f32_e32 v83, v236, v24
	v_fmac_f32_e32 v237, v236, v56
	v_mul_f32_e32 v236, v239, v55
	v_fmac_f32_e32 v236, v238, v54
	v_mul_f32_e32 v84, v239, v23
	v_add_f32_e32 v236, v237, v236
	v_fmac_f32_e32 v84, v238, v22
	v_add_f32_e32 v82, v82, v236
	ds_read_b128 v[236:239], v110 offset:12288
	v_add_f32_e32 v83, v83, v84
	v_add_f32_e32 v2, v2, v83
	s_waitcnt lgkmcnt(5)
	v_mul_f32_e32 v83, v233, v21
	v_mul_f32_e32 v233, v233, v53
	v_fmac_f32_e32 v83, v232, v20
	v_fmac_f32_e32 v233, v232, v52
	v_mul_f32_e32 v232, v235, v51
	v_fmac_f32_e32 v232, v234, v50
	v_mul_f32_e32 v84, v235, v19
	v_add_f32_e32 v232, v233, v232
	v_fmac_f32_e32 v84, v234, v18
	v_add_f32_e32 v82, v82, v232
	ds_read_b128 v[232:235], v110 offset:13312
	v_add_f32_e32 v83, v83, v84
	v_add_f32_e32 v2, v2, v83
	s_waitcnt lgkmcnt(5)
	v_mul_f32_e32 v83, v229, v49
	v_mul_f32_e32 v229, v229, v73
	v_fmac_f32_e32 v83, v228, v48
	v_fmac_f32_e32 v229, v228, v72
	v_mul_f32_e32 v228, v231, v71
	v_mul_f32_e32 v84, v231, v47
	v_fmac_f32_e32 v228, v230, v70
	v_fmac_f32_e32 v84, v230, v46
	v_add_f32_e32 v228, v229, v228
	v_add_f32_e32 v83, v83, v84
	v_add_f32_e32 v84, 0, v228
	ds_read_b128 v[228:231], v110 offset:14336
	v_add_f32_e32 v83, 0, v83
	s_waitcnt lgkmcnt(5)
	v_mul_f32_e32 v85, v225, v45
	v_mul_f32_e32 v225, v225, v81
	v_fmac_f32_e32 v85, v224, v44
	v_fmac_f32_e32 v225, v224, v80
	v_mul_f32_e32 v224, v227, v79
	v_fmac_f32_e32 v224, v226, v78
	v_mul_f32_e32 v86, v227, v43
	v_add_f32_e32 v224, v225, v224
	v_fmac_f32_e32 v86, v226, v42
	v_add_f32_e32 v84, v84, v224
	ds_read_b128 v[224:227], v110 offset:15360
	v_add_f32_e32 v85, v85, v86
	v_add_f32_e32 v83, v83, v85
	s_waitcnt lgkmcnt(5)
	v_mul_f32_e32 v85, v5, v41
	v_mul_f32_e32 v5, v5, v77
	v_fmac_f32_e32 v85, v4, v40
	v_fmac_f32_e32 v5, v4, v76
	v_mul_f32_e32 v4, v7, v75
	v_fmac_f32_e32 v4, v6, v74
	v_mul_f32_e32 v86, v7, v39
	v_add_f32_e32 v4, v5, v4
	v_fmac_f32_e32 v86, v6, v38
	v_add_f32_e32 v84, v84, v4
	ds_read_b128 v[4:7], v110 offset:16384
	v_add_f32_e32 v85, v85, v86
	v_add_f32_e32 v83, v83, v85
	s_waitcnt lgkmcnt(5)
	v_mul_f32_e32 v85, v241, v33
	v_mul_f32_e32 v241, v241, v65
	v_fmac_f32_e32 v85, v240, v32
	v_fmac_f32_e32 v241, v240, v64
	v_mul_f32_e32 v240, v243, v63
	v_fmac_f32_e32 v240, v242, v62
	v_mul_f32_e32 v86, v243, v31
	v_add_f32_e32 v240, v241, v240
	v_fmac_f32_e32 v86, v242, v30
	v_add_f32_e32 v84, v84, v240
	ds_read_b128 v[240:243], v110 offset:17408
	v_add_f32_e32 v85, v85, v86
	v_add_f32_e32 v83, v83, v85
	s_waitcnt lgkmcnt(5)
	v_mul_f32_e32 v85, v237, v37
	v_mul_f32_e32 v237, v237, v69
	v_fmac_f32_e32 v85, v236, v36
	v_fmac_f32_e32 v237, v236, v68
	v_mul_f32_e32 v236, v239, v67
	v_fmac_f32_e32 v236, v238, v66
	v_mul_f32_e32 v86, v239, v35
	v_add_f32_e32 v236, v237, v236
	v_fmac_f32_e32 v86, v238, v34
	v_add_f32_e32 v84, v84, v236
	ds_read_b128 v[236:239], v110 offset:18432
	v_add_f32_e32 v85, v85, v86
	v_add_f32_e32 v83, v83, v85
	s_waitcnt lgkmcnt(5)
	v_mul_f32_e32 v85, v233, v29
	v_mul_f32_e32 v233, v233, v61
	v_fmac_f32_e32 v85, v232, v28
	v_fmac_f32_e32 v233, v232, v60
	v_mul_f32_e32 v232, v235, v59
	v_fmac_f32_e32 v232, v234, v58
	v_mul_f32_e32 v86, v235, v27
	v_add_f32_e32 v232, v233, v232
	v_fmac_f32_e32 v86, v234, v26
	v_add_f32_e32 v84, v84, v232
	ds_read_b128 v[232:235], v110 offset:19456
	v_add_f32_e32 v85, v85, v86
	v_add_f32_e32 v83, v83, v85
	s_waitcnt lgkmcnt(5)
	v_mul_f32_e32 v85, v229, v25
	v_mul_f32_e32 v229, v229, v57
	v_fmac_f32_e32 v85, v228, v24
	v_fmac_f32_e32 v229, v228, v56
	v_mul_f32_e32 v228, v231, v55
	v_fmac_f32_e32 v228, v230, v54
	v_mul_f32_e32 v86, v231, v23
	v_add_f32_e32 v228, v229, v228
	v_fmac_f32_e32 v86, v230, v22
	v_add_f32_e32 v84, v84, v228
	ds_read_b128 v[228:231], v110 offset:20480
	v_add_f32_e32 v85, v85, v86
	v_add_f32_e32 v83, v83, v85
	s_waitcnt lgkmcnt(5)
	v_mul_f32_e32 v85, v225, v21
	v_mul_f32_e32 v225, v225, v53
	v_fmac_f32_e32 v85, v224, v20
	v_fmac_f32_e32 v225, v224, v52
	v_mul_f32_e32 v224, v227, v51
	v_fmac_f32_e32 v224, v226, v50
	v_mul_f32_e32 v86, v227, v19
	v_add_f32_e32 v224, v225, v224
	v_fmac_f32_e32 v86, v226, v18
	v_add_f32_e32 v84, v84, v224
	ds_read_b128 v[224:227], v110 offset:21504
	v_add_f32_e32 v85, v85, v86
	v_add_f32_e32 v83, v83, v85
	s_waitcnt lgkmcnt(5)
	v_mul_f32_e32 v85, v5, v49
	v_mul_f32_e32 v5, v5, v73
	v_fmac_f32_e32 v85, v4, v48
	v_fmac_f32_e32 v5, v4, v72
	v_mul_f32_e32 v4, v7, v71
	v_mul_f32_e32 v86, v7, v47
	v_fmac_f32_e32 v4, v6, v70
	v_fmac_f32_e32 v86, v6, v46
	v_add_f32_e32 v4, v5, v4
	v_add_f32_e32 v85, v85, v86
	v_add_f32_e32 v86, 0, v4
	ds_read_b128 v[4:7], v110 offset:22528
	v_add_f32_e32 v85, 0, v85
	s_waitcnt lgkmcnt(5)
	v_mul_f32_e32 v87, v241, v45
	v_mul_f32_e32 v241, v241, v81
	v_fmac_f32_e32 v87, v240, v44
	v_fmac_f32_e32 v241, v240, v80
	v_mul_f32_e32 v240, v243, v79
	v_fmac_f32_e32 v240, v242, v78
	v_mul_f32_e32 v88, v243, v43
	v_add_f32_e32 v240, v241, v240
	v_fmac_f32_e32 v88, v242, v42
	v_add_f32_e32 v86, v86, v240
	ds_read_b128 v[240:243], v110 offset:23552
	v_add_f32_e32 v87, v87, v88
	v_add_f32_e32 v85, v85, v87
	s_waitcnt lgkmcnt(5)
	v_mul_f32_e32 v87, v237, v41
	v_mul_f32_e32 v237, v237, v77
	v_fmac_f32_e32 v87, v236, v40
	v_fmac_f32_e32 v237, v236, v76
	v_mul_f32_e32 v236, v239, v75
	v_fmac_f32_e32 v236, v238, v74
	v_mul_f32_e32 v88, v239, v39
	v_add_f32_e32 v236, v237, v236
	v_fmac_f32_e32 v88, v238, v38
	v_add_f32_e32 v86, v86, v236
	ds_read_b128 v[236:239], v110 offset:24576
	v_add_f32_e32 v87, v87, v88
	v_add_f32_e32 v85, v85, v87
	s_waitcnt lgkmcnt(5)
	v_mul_f32_e32 v87, v233, v33
	v_mul_f32_e32 v233, v233, v65
	v_fmac_f32_e32 v87, v232, v32
	v_fmac_f32_e32 v233, v232, v64
	v_mul_f32_e32 v232, v235, v63
	v_fmac_f32_e32 v232, v234, v62
	v_mul_f32_e32 v88, v235, v31
	v_add_f32_e32 v232, v233, v232
	v_fmac_f32_e32 v88, v234, v30
	v_add_f32_e32 v86, v86, v232
	ds_read_b128 v[232:235], v110 offset:25600
	v_add_f32_e32 v87, v87, v88
	v_add_f32_e32 v85, v85, v87
	s_waitcnt lgkmcnt(5)
	v_mul_f32_e32 v87, v229, v37
	v_mul_f32_e32 v229, v229, v69
	v_fmac_f32_e32 v87, v228, v36
	v_fmac_f32_e32 v229, v228, v68
	v_mul_f32_e32 v228, v231, v67
	v_fmac_f32_e32 v228, v230, v66
	v_mul_f32_e32 v88, v231, v35
	v_add_f32_e32 v228, v229, v228
	v_fmac_f32_e32 v88, v230, v34
	v_add_f32_e32 v86, v86, v228
	ds_read_b128 v[228:231], v110 offset:26624
	v_add_f32_e32 v87, v87, v88
	v_add_f32_e32 v85, v85, v87
	s_waitcnt lgkmcnt(5)
	v_mul_f32_e32 v87, v225, v29
	v_mul_f32_e32 v225, v225, v61
	v_fmac_f32_e32 v87, v224, v28
	v_fmac_f32_e32 v225, v224, v60
	v_mul_f32_e32 v224, v227, v59
	v_fmac_f32_e32 v224, v226, v58
	v_mul_f32_e32 v88, v227, v27
	v_add_f32_e32 v224, v225, v224
	v_fmac_f32_e32 v88, v226, v26
	v_add_f32_e32 v86, v86, v224
	ds_read_b128 v[224:227], v110 offset:27648
	v_add_f32_e32 v87, v87, v88
	v_add_f32_e32 v85, v85, v87
	s_waitcnt lgkmcnt(5)
	v_mul_f32_e32 v87, v5, v25
	v_mul_f32_e32 v5, v5, v57
	v_fmac_f32_e32 v87, v4, v24
	v_fmac_f32_e32 v5, v4, v56
	v_mul_f32_e32 v4, v7, v55
	v_fmac_f32_e32 v4, v6, v54
	v_mul_f32_e32 v88, v7, v23
	v_add_f32_e32 v4, v5, v4
	v_fmac_f32_e32 v88, v6, v22
	v_add_f32_e32 v86, v86, v4
	ds_read_b128 v[4:7], v110 offset:28672
	v_add_f32_e32 v87, v87, v88
	v_add_f32_e32 v85, v85, v87
	s_waitcnt lgkmcnt(5)
	v_mul_f32_e32 v87, v241, v21
	v_mul_f32_e32 v241, v241, v53
	v_fmac_f32_e32 v87, v240, v20
	v_fmac_f32_e32 v241, v240, v52
	v_mul_f32_e32 v240, v243, v51
	v_fmac_f32_e32 v240, v242, v50
	v_mul_f32_e32 v88, v243, v19
	v_add_f32_e32 v240, v241, v240
	v_fmac_f32_e32 v88, v242, v18
	v_add_f32_e32 v86, v86, v240
	ds_read_b128 v[240:243], v110 offset:29696
	v_add_f32_e32 v87, v87, v88
	v_add_f32_e32 v85, v85, v87
	s_waitcnt lgkmcnt(5)
	v_mul_f32_e32 v87, v237, v49
	v_mul_f32_e32 v237, v237, v73
	v_fmac_f32_e32 v87, v236, v48
	v_fmac_f32_e32 v237, v236, v72
	v_mul_f32_e32 v236, v239, v71
	v_mul_f32_e32 v88, v239, v47
	v_fmac_f32_e32 v236, v238, v70
	v_fmac_f32_e32 v88, v238, v46
	v_add_f32_e32 v236, v237, v236
	v_add_f32_e32 v87, v87, v88
	v_add_f32_e32 v88, 0, v236
	ds_read_b128 v[236:239], v110 offset:30720
	v_add_f32_e32 v87, 0, v87
	s_waitcnt lgkmcnt(5)
	v_mul_f32_e32 v89, v233, v45
	v_mul_f32_e32 v233, v233, v81
	v_fmac_f32_e32 v89, v232, v44
	v_fmac_f32_e32 v233, v232, v80
	v_mul_f32_e32 v232, v235, v79
	v_fmac_f32_e32 v232, v234, v78
	v_mul_f32_e32 v90, v235, v43
	v_add_f32_e32 v232, v233, v232
	v_fmac_f32_e32 v90, v234, v42
	v_add_f32_e32 v88, v88, v232
	ds_read_b128 v[232:235], v110 offset:31744
	v_add_f32_e32 v89, v89, v90
	v_add_f32_e32 v87, v87, v89
	s_waitcnt lgkmcnt(5)
	v_mul_f32_e32 v89, v229, v41
	v_mul_f32_e32 v229, v229, v77
	v_fmac_f32_e32 v89, v228, v40
	v_fmac_f32_e32 v229, v228, v76
	v_mul_f32_e32 v228, v231, v75
	v_fmac_f32_e32 v228, v230, v74
	v_mul_f32_e32 v90, v231, v39
	v_add_f32_e32 v228, v229, v228
	v_fmac_f32_e32 v90, v230, v38
	v_add_f32_e32 v88, v88, v228
	ds_read_b128 v[228:231], v110 offset:32768
	v_add_f32_e32 v89, v89, v90
	v_add_f32_e32 v87, v87, v89
	s_waitcnt lgkmcnt(5)
	v_mul_f32_e32 v89, v225, v33
	v_mul_f32_e32 v225, v225, v65
	v_fmac_f32_e32 v89, v224, v32
	v_fmac_f32_e32 v225, v224, v64
	v_mul_f32_e32 v224, v227, v63
	v_fmac_f32_e32 v224, v226, v62
	v_mul_f32_e32 v90, v227, v31
	v_add_f32_e32 v224, v225, v224
	v_fmac_f32_e32 v90, v226, v30
	v_add_f32_e32 v88, v88, v224
	ds_read_b128 v[224:227], v110 offset:33792
	v_add_f32_e32 v89, v89, v90
	v_add_f32_e32 v87, v87, v89
	s_waitcnt lgkmcnt(5)
	v_mul_f32_e32 v89, v5, v37
	v_mul_f32_e32 v5, v5, v69
	v_fmac_f32_e32 v89, v4, v36
	v_fmac_f32_e32 v5, v4, v68
	v_mul_f32_e32 v4, v7, v67
	v_fmac_f32_e32 v4, v6, v66
	v_mul_f32_e32 v90, v7, v35
	v_add_f32_e32 v4, v5, v4
	v_fmac_f32_e32 v90, v6, v34
	v_add_f32_e32 v88, v88, v4
	ds_read_b128 v[4:7], v110 offset:34816
	v_add_f32_e32 v89, v89, v90
	v_add_f32_e32 v87, v87, v89
	s_waitcnt lgkmcnt(5)
	v_mul_f32_e32 v89, v241, v29
	v_mul_f32_e32 v241, v241, v61
	v_fmac_f32_e32 v89, v240, v28
	v_fmac_f32_e32 v241, v240, v60
	v_mul_f32_e32 v240, v243, v59
	v_fmac_f32_e32 v240, v242, v58
	v_mul_f32_e32 v90, v243, v27
	v_add_f32_e32 v240, v241, v240
	v_fmac_f32_e32 v90, v242, v26
	v_add_f32_e32 v88, v88, v240
	ds_read_b128 v[240:243], v110 offset:35840
	v_add_f32_e32 v89, v89, v90
	v_add_f32_e32 v87, v87, v89
	s_waitcnt lgkmcnt(5)
	v_mul_f32_e32 v89, v237, v25
	v_mul_f32_e32 v237, v237, v57
	v_fmac_f32_e32 v89, v236, v24
	v_fmac_f32_e32 v237, v236, v56
	v_mul_f32_e32 v236, v239, v55
	v_fmac_f32_e32 v236, v238, v54
	v_mul_f32_e32 v90, v239, v23
	v_add_f32_e32 v236, v237, v236
	v_fmac_f32_e32 v90, v238, v22
	v_add_f32_e32 v88, v88, v236
	ds_read_b128 v[236:239], v110 offset:36864
	v_add_f32_e32 v89, v89, v90
	v_add_f32_e32 v87, v87, v89
	s_waitcnt lgkmcnt(5)
	v_mul_f32_e32 v89, v233, v21
	v_mul_f32_e32 v233, v233, v53
	v_fmac_f32_e32 v89, v232, v20
	v_fmac_f32_e32 v233, v232, v52
	v_mul_f32_e32 v232, v235, v51
	v_fmac_f32_e32 v232, v234, v50
	v_mul_f32_e32 v90, v235, v19
	v_add_f32_e32 v232, v233, v232
	v_fmac_f32_e32 v90, v234, v18
	v_add_f32_e32 v88, v88, v232
	ds_read_b128 v[232:235], v110 offset:37888
	v_add_f32_e32 v89, v89, v90
	v_add_f32_e32 v87, v87, v89
	s_waitcnt lgkmcnt(5)
	v_mul_f32_e32 v89, v229, v49
	v_mul_f32_e32 v229, v229, v73
	v_fmac_f32_e32 v89, v228, v48
	v_fmac_f32_e32 v229, v228, v72
	v_mul_f32_e32 v228, v231, v71
	v_mul_f32_e32 v90, v231, v47
	v_fmac_f32_e32 v228, v230, v70
	v_fmac_f32_e32 v90, v230, v46
	v_add_f32_e32 v228, v229, v228
	v_add_f32_e32 v89, v89, v90
	v_add_f32_e32 v90, 0, v228
	ds_read_b128 v[228:231], v110 offset:38912
	v_add_f32_e32 v89, 0, v89
	s_waitcnt lgkmcnt(5)
	v_mul_f32_e32 v91, v225, v45
	v_mul_f32_e32 v225, v225, v81
	v_fmac_f32_e32 v91, v224, v44
	v_fmac_f32_e32 v225, v224, v80
	v_mul_f32_e32 v224, v227, v79
	v_fmac_f32_e32 v224, v226, v78
	v_mul_f32_e32 v92, v227, v43
	v_add_f32_e32 v224, v225, v224
	v_fmac_f32_e32 v92, v226, v42
	v_add_f32_e32 v90, v90, v224
	ds_read_b128 v[224:227], v110 offset:39936
	v_add_f32_e32 v91, v91, v92
	v_add_f32_e32 v89, v89, v91
	s_waitcnt lgkmcnt(5)
	v_mul_f32_e32 v91, v5, v41
	v_mul_f32_e32 v5, v5, v77
	v_fmac_f32_e32 v91, v4, v40
	v_fmac_f32_e32 v5, v4, v76
	v_mul_f32_e32 v4, v7, v75
	v_fmac_f32_e32 v4, v6, v74
	v_mul_f32_e32 v92, v7, v39
	v_add_f32_e32 v4, v5, v4
	v_fmac_f32_e32 v92, v6, v38
	v_add_f32_e32 v90, v90, v4
	ds_read_b128 v[4:7], v110 offset:40960
	v_add_f32_e32 v91, v91, v92
	v_add_f32_e32 v89, v89, v91
	s_waitcnt lgkmcnt(5)
	v_mul_f32_e32 v91, v241, v33
	v_mul_f32_e32 v241, v241, v65
	v_fmac_f32_e32 v91, v240, v32
	v_fmac_f32_e32 v241, v240, v64
	v_mul_f32_e32 v240, v243, v63
	v_fmac_f32_e32 v240, v242, v62
	v_mul_f32_e32 v92, v243, v31
	v_add_f32_e32 v240, v241, v240
	v_fmac_f32_e32 v92, v242, v30
	v_add_f32_e32 v90, v90, v240
	ds_read_b128 v[240:243], v110 offset:41984
	v_add_f32_e32 v91, v91, v92
	v_add_f32_e32 v89, v89, v91
	s_waitcnt lgkmcnt(5)
	v_mul_f32_e32 v91, v237, v37
	v_mul_f32_e32 v237, v237, v69
	v_fmac_f32_e32 v91, v236, v36
	v_fmac_f32_e32 v237, v236, v68
	v_mul_f32_e32 v236, v239, v67
	v_fmac_f32_e32 v236, v238, v66
	v_mul_f32_e32 v92, v239, v35
	v_add_f32_e32 v236, v237, v236
	v_fmac_f32_e32 v92, v238, v34
	v_add_f32_e32 v90, v90, v236
	ds_read_b128 v[236:239], v110 offset:43008
	v_add_f32_e32 v91, v91, v92
	v_add_f32_e32 v89, v89, v91
	s_waitcnt lgkmcnt(5)
	v_mul_f32_e32 v91, v233, v29
	v_mul_f32_e32 v233, v233, v61
	v_fmac_f32_e32 v91, v232, v28
	v_fmac_f32_e32 v233, v232, v60
	v_mul_f32_e32 v232, v235, v59
	v_fmac_f32_e32 v232, v234, v58
	v_mul_f32_e32 v92, v235, v27
	v_add_f32_e32 v232, v233, v232
	v_fmac_f32_e32 v92, v234, v26
	v_add_f32_e32 v90, v90, v232
	ds_read_b128 v[232:235], v110 offset:44032
	v_add_f32_e32 v91, v91, v92
	v_add_f32_e32 v89, v89, v91
	s_waitcnt lgkmcnt(5)
	v_mul_f32_e32 v91, v229, v25
	v_mul_f32_e32 v229, v229, v57
	v_fmac_f32_e32 v91, v228, v24
	v_fmac_f32_e32 v229, v228, v56
	v_mul_f32_e32 v228, v231, v55
	v_fmac_f32_e32 v228, v230, v54
	v_mul_f32_e32 v92, v231, v23
	v_add_f32_e32 v228, v229, v228
	v_fmac_f32_e32 v92, v230, v22
	v_add_f32_e32 v90, v90, v228
	ds_read_b128 v[228:231], v110 offset:45056
	v_add_f32_e32 v91, v91, v92
	v_add_f32_e32 v89, v89, v91
	s_waitcnt lgkmcnt(5)
	v_mul_f32_e32 v91, v225, v21
	v_mul_f32_e32 v225, v225, v53
	v_fmac_f32_e32 v91, v224, v20
	v_fmac_f32_e32 v225, v224, v52
	v_mul_f32_e32 v224, v227, v51
	v_fmac_f32_e32 v224, v226, v50
	v_mul_f32_e32 v92, v227, v19
	v_add_f32_e32 v224, v225, v224
	v_fmac_f32_e32 v92, v226, v18
	v_add_f32_e32 v90, v90, v224
	ds_read_b128 v[224:227], v110 offset:46080
	v_add_f32_e32 v91, v91, v92
	v_add_f32_e32 v89, v89, v91
	s_waitcnt lgkmcnt(5)
	v_mul_f32_e32 v91, v5, v49
	v_mul_f32_e32 v5, v5, v73
	v_fmac_f32_e32 v91, v4, v48
	v_fmac_f32_e32 v5, v4, v72
	v_mul_f32_e32 v4, v7, v71
	v_mul_f32_e32 v92, v7, v47
	v_fmac_f32_e32 v4, v6, v70
	v_fmac_f32_e32 v92, v6, v46
	v_add_f32_e32 v4, v5, v4
	v_add_f32_e32 v91, v91, v92
	v_add_f32_e32 v92, 0, v4
	ds_read_b128 v[4:7], v110 offset:47104
	v_add_f32_e32 v91, 0, v91
	s_waitcnt lgkmcnt(5)
	v_mul_f32_e32 v93, v241, v45
	v_mul_f32_e32 v241, v241, v81
	v_fmac_f32_e32 v93, v240, v44
	v_fmac_f32_e32 v241, v240, v80
	v_mul_f32_e32 v240, v243, v79
	v_fmac_f32_e32 v240, v242, v78
	v_mul_f32_e32 v94, v243, v43
	v_add_f32_e32 v240, v241, v240
	v_fmac_f32_e32 v94, v242, v42
	v_add_f32_e32 v92, v92, v240
	ds_read_b128 v[240:243], v110 offset:48128
	v_add_f32_e32 v93, v93, v94
	v_add_f32_e32 v91, v91, v93
	s_waitcnt lgkmcnt(5)
	v_mul_f32_e32 v93, v237, v41
	v_mul_f32_e32 v237, v237, v77
	v_fmac_f32_e32 v93, v236, v40
	v_fmac_f32_e32 v237, v236, v76
	v_mul_f32_e32 v236, v239, v75
	v_fmac_f32_e32 v236, v238, v74
	v_mul_f32_e32 v94, v239, v39
	v_add_f32_e32 v236, v237, v236
	v_fmac_f32_e32 v94, v238, v38
	v_add_f32_e32 v92, v92, v236
	ds_read_b128 v[236:239], v110 offset:49152
	v_add_f32_e32 v93, v93, v94
	v_add_f32_e32 v91, v91, v93
	s_waitcnt lgkmcnt(5)
	v_mul_f32_e32 v93, v233, v33
	v_mul_f32_e32 v233, v233, v65
	v_fmac_f32_e32 v93, v232, v32
	v_fmac_f32_e32 v233, v232, v64
	v_mul_f32_e32 v232, v235, v63
	v_fmac_f32_e32 v232, v234, v62
	v_mul_f32_e32 v94, v235, v31
	v_add_f32_e32 v232, v233, v232
	v_fmac_f32_e32 v94, v234, v30
	v_add_f32_e32 v92, v92, v232
	ds_read_b128 v[232:235], v110 offset:50176
	v_add_f32_e32 v93, v93, v94
	v_add_f32_e32 v91, v91, v93
	s_waitcnt lgkmcnt(5)
	v_mul_f32_e32 v93, v229, v37
	v_mul_f32_e32 v229, v229, v69
	v_fmac_f32_e32 v93, v228, v36
	v_fmac_f32_e32 v229, v228, v68
	v_mul_f32_e32 v228, v231, v67
	v_fmac_f32_e32 v228, v230, v66
	v_mul_f32_e32 v94, v231, v35
	v_add_f32_e32 v228, v229, v228
	v_fmac_f32_e32 v94, v230, v34
	v_add_f32_e32 v92, v92, v228
	ds_read_b128 v[228:231], v110 offset:51200
	v_add_f32_e32 v93, v93, v94
	v_add_f32_e32 v91, v91, v93
	s_waitcnt lgkmcnt(5)
	v_mul_f32_e32 v93, v225, v29
	v_mul_f32_e32 v225, v225, v61
	v_fmac_f32_e32 v93, v224, v28
	v_fmac_f32_e32 v225, v224, v60
	v_mul_f32_e32 v224, v227, v59
	v_fmac_f32_e32 v224, v226, v58
	v_mul_f32_e32 v94, v227, v27
	v_add_f32_e32 v224, v225, v224
	v_fmac_f32_e32 v94, v226, v26
	v_add_f32_e32 v92, v92, v224
	ds_read_b128 v[224:227], v110 offset:52224
	v_add_f32_e32 v93, v93, v94
	v_add_f32_e32 v91, v91, v93
	s_waitcnt lgkmcnt(5)
	v_mul_f32_e32 v93, v5, v25
	v_mul_f32_e32 v5, v5, v57
	v_fmac_f32_e32 v93, v4, v24
	v_fmac_f32_e32 v5, v4, v56
	v_mul_f32_e32 v4, v7, v55
	v_fmac_f32_e32 v4, v6, v54
	v_mul_f32_e32 v94, v7, v23
	v_add_f32_e32 v4, v5, v4
	v_fmac_f32_e32 v94, v6, v22
	v_add_f32_e32 v92, v92, v4
	ds_read_b128 v[4:7], v110 offset:53248
	v_add_f32_e32 v93, v93, v94
	v_add_f32_e32 v91, v91, v93
	s_waitcnt lgkmcnt(5)
	v_mul_f32_e32 v93, v241, v21
	v_mul_f32_e32 v241, v241, v53
	v_fmac_f32_e32 v93, v240, v20
	v_fmac_f32_e32 v241, v240, v52
	v_mul_f32_e32 v240, v243, v51
	v_fmac_f32_e32 v240, v242, v50
	v_mul_f32_e32 v94, v243, v19
	v_add_f32_e32 v240, v241, v240
	v_fmac_f32_e32 v94, v242, v18
	v_add_f32_e32 v92, v92, v240
	ds_read_b128 v[240:243], v110 offset:54272
	v_add_f32_e32 v93, v93, v94
	v_add_f32_e32 v91, v91, v93
	s_waitcnt lgkmcnt(5)
	v_mul_f32_e32 v93, v237, v49
	v_mul_f32_e32 v237, v237, v73
	v_fmac_f32_e32 v93, v236, v48
	v_fmac_f32_e32 v237, v236, v72
	v_mul_f32_e32 v236, v239, v71
	v_mul_f32_e32 v94, v239, v47
	v_fmac_f32_e32 v236, v238, v70
	v_fmac_f32_e32 v94, v238, v46
	v_add_f32_e32 v236, v237, v236
	v_add_f32_e32 v93, v93, v94
	v_add_f32_e32 v94, 0, v236
	ds_read_b128 v[236:239], v110 offset:55296
	v_add_f32_e32 v93, 0, v93
	s_waitcnt lgkmcnt(5)
	v_mul_f32_e32 v95, v233, v45
	v_mul_f32_e32 v233, v233, v81
	v_fmac_f32_e32 v95, v232, v44
	v_fmac_f32_e32 v233, v232, v80
	v_mul_f32_e32 v232, v235, v79
	v_fmac_f32_e32 v232, v234, v78
	v_mul_f32_e32 v96, v235, v43
	v_add_f32_e32 v232, v233, v232
	v_fmac_f32_e32 v96, v234, v42
	v_add_f32_e32 v94, v94, v232
	ds_read_b128 v[232:235], v110 offset:56320
	v_add_f32_e32 v95, v95, v96
	v_add_f32_e32 v93, v93, v95
	s_waitcnt lgkmcnt(5)
	v_mul_f32_e32 v95, v229, v41
	v_mul_f32_e32 v229, v229, v77
	v_fmac_f32_e32 v95, v228, v40
	v_fmac_f32_e32 v229, v228, v76
	v_mul_f32_e32 v228, v231, v75
	v_fmac_f32_e32 v228, v230, v74
	v_mul_f32_e32 v96, v231, v39
	v_add_f32_e32 v228, v229, v228
	v_fmac_f32_e32 v96, v230, v38
	v_add_f32_e32 v94, v94, v228
	ds_read_b128 v[228:231], v110 offset:57344
	v_add_f32_e32 v95, v95, v96
	v_add_f32_e32 v93, v93, v95
	s_waitcnt lgkmcnt(5)
	v_mul_f32_e32 v95, v225, v33
	v_mul_f32_e32 v225, v225, v65
	v_fmac_f32_e32 v95, v224, v32
	v_fmac_f32_e32 v225, v224, v64
	v_mul_f32_e32 v224, v227, v63
	v_fmac_f32_e32 v224, v226, v62
	v_mul_f32_e32 v96, v227, v31
	v_add_f32_e32 v224, v225, v224
	v_fmac_f32_e32 v96, v226, v30
	v_add_f32_e32 v94, v94, v224
	ds_read_b128 v[224:227], v110 offset:58368
	v_add_f32_e32 v95, v95, v96
	v_add_f32_e32 v93, v93, v95
	s_waitcnt lgkmcnt(5)
	v_mul_f32_e32 v95, v5, v37
	v_mul_f32_e32 v5, v5, v69
	v_fmac_f32_e32 v95, v4, v36
	v_fmac_f32_e32 v5, v4, v68
	v_mul_f32_e32 v4, v7, v67
	v_fmac_f32_e32 v4, v6, v66
	v_mul_f32_e32 v96, v7, v35
	v_add_f32_e32 v4, v5, v4
	v_fmac_f32_e32 v96, v6, v34
	v_add_f32_e32 v94, v94, v4
	ds_read_b128 v[4:7], v110 offset:59392
	v_add_f32_e32 v95, v95, v96
	v_add_f32_e32 v93, v93, v95
	s_waitcnt lgkmcnt(5)
	v_mul_f32_e32 v95, v241, v29
	v_mul_f32_e32 v241, v241, v61
	v_fmac_f32_e32 v95, v240, v28
	v_fmac_f32_e32 v241, v240, v60
	v_mul_f32_e32 v240, v243, v59
	v_fmac_f32_e32 v240, v242, v58
	v_mul_f32_e32 v96, v243, v27
	v_add_f32_e32 v240, v241, v240
	v_fmac_f32_e32 v96, v242, v26
	v_add_f32_e32 v94, v94, v240
	ds_read_b128 v[240:243], v110 offset:60416
	v_add_f32_e32 v95, v95, v96
	v_add_f32_e32 v93, v93, v95
	s_waitcnt lgkmcnt(5)
	v_mul_f32_e32 v95, v237, v25
	v_mul_f32_e32 v237, v237, v57
	v_fmac_f32_e32 v95, v236, v24
	v_fmac_f32_e32 v237, v236, v56
	v_mul_f32_e32 v236, v239, v55
	v_fmac_f32_e32 v236, v238, v54
	v_mul_f32_e32 v96, v239, v23
	v_add_f32_e32 v236, v237, v236
	v_fmac_f32_e32 v96, v238, v22
	v_add_f32_e32 v94, v94, v236
	ds_read_b128 v[236:239], v110 offset:61440
	v_add_f32_e32 v95, v95, v96
	v_add_f32_e32 v93, v93, v95
	s_waitcnt lgkmcnt(5)
	v_mul_f32_e32 v95, v233, v21
	v_mul_f32_e32 v233, v233, v53
	v_fmac_f32_e32 v95, v232, v20
	v_fmac_f32_e32 v233, v232, v52
	v_mul_f32_e32 v232, v235, v51
	v_fmac_f32_e32 v232, v234, v50
	v_mul_f32_e32 v96, v235, v19
	v_add_f32_e32 v232, v233, v232
	v_fmac_f32_e32 v96, v234, v18
	v_add_f32_e32 v94, v94, v232
	ds_read_b128 v[232:235], v110 offset:62464
	v_add_f32_e32 v95, v95, v96
	v_add_f32_e32 v93, v93, v95
	s_waitcnt lgkmcnt(5)
	v_mul_f32_e32 v95, v229, v49
	v_mul_f32_e32 v229, v229, v73
	v_fmac_f32_e32 v95, v228, v48
	v_fmac_f32_e32 v229, v228, v72
	v_mul_f32_e32 v228, v231, v71
	v_mul_f32_e32 v96, v231, v47
	v_fmac_f32_e32 v228, v230, v70
	v_fmac_f32_e32 v96, v230, v46
	v_add_f32_e32 v228, v229, v228
	v_add_f32_e32 v95, v95, v96
	v_add_f32_e32 v96, 0, v228
	ds_read_b128 v[228:231], v110 offset:63488
	v_add_f32_e32 v95, 0, v95
	s_waitcnt lgkmcnt(5)
	v_mul_f32_e32 v97, v225, v45
	v_mul_f32_e32 v225, v225, v81
	v_fmac_f32_e32 v97, v224, v44
	v_fmac_f32_e32 v225, v224, v80
	v_mul_f32_e32 v224, v227, v79
	v_fmac_f32_e32 v224, v226, v78
	v_mul_f32_e32 v98, v227, v43
	v_add_f32_e32 v224, v225, v224
	v_fmac_f32_e32 v98, v226, v42
	v_add_f32_e32 v96, v96, v224
	ds_read_b128 v[224:227], v110 offset:64512
	v_add_f32_e32 v97, v97, v98
	v_add_f32_e32 v95, v95, v97
	s_waitcnt lgkmcnt(5)
	v_mul_f32_e32 v97, v5, v41
	v_mul_f32_e32 v5, v5, v77
	v_fmac_f32_e32 v97, v4, v40
	v_fmac_f32_e32 v5, v4, v76
	v_mul_f32_e32 v4, v7, v75
	v_fmac_f32_e32 v4, v6, v74
	v_mul_f32_e32 v98, v7, v39
	v_add_f32_e32 v4, v5, v4
	v_fmac_f32_e32 v98, v6, v38
	v_add_f32_e32 v96, v96, v4
	ds_read_b128 v[4:7], v117
	v_add_f32_e32 v97, v97, v98
	v_add_f32_e32 v95, v95, v97
	s_waitcnt lgkmcnt(5)
	v_mul_f32_e32 v97, v241, v33
	v_mul_f32_e32 v241, v241, v65
	v_fmac_f32_e32 v97, v240, v32
	v_fmac_f32_e32 v241, v240, v64
	v_mul_f32_e32 v240, v243, v63
	v_fmac_f32_e32 v240, v242, v62
	v_mul_f32_e32 v98, v243, v31
	v_add_f32_e32 v240, v241, v240
	v_fmac_f32_e32 v98, v242, v30
	v_add_f32_e32 v96, v96, v240
	ds_read_b128 v[240:243], v118
	v_add_f32_e32 v97, v97, v98
	v_add_f32_e32 v95, v95, v97
	s_waitcnt lgkmcnt(5)
	v_mul_f32_e32 v97, v237, v37
	v_mul_f32_e32 v237, v237, v69
	v_fmac_f32_e32 v97, v236, v36
	v_fmac_f32_e32 v237, v236, v68
	v_mul_f32_e32 v236, v239, v67
	v_fmac_f32_e32 v236, v238, v66
	v_mul_f32_e32 v98, v239, v35
	v_add_f32_e32 v236, v237, v236
	v_fmac_f32_e32 v98, v238, v34
	v_add_f32_e32 v96, v96, v236
	ds_read_b128 v[236:239], v119
	v_add_f32_e32 v97, v97, v98
	v_add_f32_e32 v95, v95, v97
	s_waitcnt lgkmcnt(5)
	v_mul_f32_e32 v97, v233, v29
	v_mul_f32_e32 v233, v233, v61
	v_fmac_f32_e32 v97, v232, v28
	v_fmac_f32_e32 v233, v232, v60
	v_mul_f32_e32 v232, v235, v59
	v_fmac_f32_e32 v232, v234, v58
	v_mul_f32_e32 v98, v235, v27
	v_add_f32_e32 v232, v233, v232
	v_fmac_f32_e32 v98, v234, v26
	v_add_f32_e32 v96, v96, v232
	ds_read_b128 v[232:235], v120
	v_add_f32_e32 v97, v97, v98
	v_add_f32_e32 v95, v95, v97
	s_waitcnt lgkmcnt(5)
	v_mul_f32_e32 v97, v229, v25
	v_mul_f32_e32 v229, v229, v57
	v_fmac_f32_e32 v97, v228, v24
	v_fmac_f32_e32 v229, v228, v56
	v_mul_f32_e32 v228, v231, v55
	v_fmac_f32_e32 v228, v230, v54
	v_mul_f32_e32 v98, v231, v23
	v_add_f32_e32 v228, v229, v228
	v_fmac_f32_e32 v98, v230, v22
	v_add_f32_e32 v96, v96, v228
	ds_read_b128 v[228:231], v121
	v_add_f32_e32 v97, v97, v98
	v_add_f32_e32 v95, v95, v97
	s_waitcnt lgkmcnt(5)
	v_mul_f32_e32 v97, v225, v21
	v_mul_f32_e32 v225, v225, v53
	v_fmac_f32_e32 v97, v224, v20
	v_fmac_f32_e32 v225, v224, v52
	v_mul_f32_e32 v224, v227, v51
	v_fmac_f32_e32 v224, v226, v50
	v_mul_f32_e32 v98, v227, v19
	v_add_f32_e32 v224, v225, v224
	v_fmac_f32_e32 v98, v226, v18
	v_add_f32_e32 v96, v96, v224
	ds_read_b128 v[224:227], v122
	v_add_f32_e32 v97, v97, v98
	v_add_f32_e32 v95, v95, v97
	s_waitcnt lgkmcnt(5)
	v_mul_f32_e32 v97, v5, v49
	v_mul_f32_e32 v5, v5, v73
	v_fmac_f32_e32 v97, v4, v48
	v_fmac_f32_e32 v5, v4, v72
	v_mul_f32_e32 v4, v7, v71
	v_mul_f32_e32 v98, v7, v47
	v_fmac_f32_e32 v4, v6, v70
	v_fmac_f32_e32 v98, v6, v46
	v_add_f32_e32 v4, v5, v4
	v_add_f32_e32 v97, v97, v98
	v_add_f32_e32 v98, 0, v4
	ds_read_b128 v[4:7], v123
	v_add_f32_e32 v97, 0, v97
	s_waitcnt lgkmcnt(5)
	v_mul_f32_e32 v99, v241, v45
	v_mul_f32_e32 v241, v241, v81
	v_fmac_f32_e32 v99, v240, v44
	v_fmac_f32_e32 v241, v240, v80
	v_mul_f32_e32 v240, v243, v79
	v_fmac_f32_e32 v240, v242, v78
	v_mul_f32_e32 v100, v243, v43
	v_add_f32_e32 v240, v241, v240
	v_fmac_f32_e32 v100, v242, v42
	v_add_f32_e32 v98, v98, v240
	v_add_f32_e32 v99, v99, v100
	v_add_f32_e32 v97, v97, v99
	s_waitcnt lgkmcnt(4)
	v_mul_f32_e32 v99, v237, v41
	v_mul_f32_e32 v237, v237, v77
	v_fmac_f32_e32 v99, v236, v40
	v_fmac_f32_e32 v237, v236, v76
	v_mul_f32_e32 v236, v239, v75
	v_fmac_f32_e32 v236, v238, v74
	v_mul_f32_e32 v100, v239, v39
	v_add_f32_e32 v236, v237, v236
	v_fmac_f32_e32 v100, v238, v38
	v_add_f32_e32 v98, v98, v236
	v_add_f32_e32 v99, v99, v100
	v_add_f32_e32 v97, v97, v99
	s_waitcnt lgkmcnt(3)
	v_mul_f32_e32 v99, v233, v33
	v_mul_f32_e32 v233, v233, v65
	v_fmac_f32_e32 v99, v232, v32
	v_mul_f32_e32 v100, v235, v31
	v_fmac_f32_e32 v233, v232, v64
	v_mul_f32_e32 v232, v235, v63
	v_fmac_f32_e32 v100, v234, v30
	v_fmac_f32_e32 v232, v234, v62
	v_add_f32_e32 v99, v99, v100
	v_add_f32_e32 v232, v233, v232
	v_add_f32_e32 v97, v97, v99
	v_add_f32_e32 v99, v98, v232
	s_waitcnt lgkmcnt(2)
	v_mul_f32_e32 v98, v229, v37
	v_mul_f32_e32 v229, v229, v69
	v_fmac_f32_e32 v98, v228, v36
	v_mul_f32_e32 v100, v231, v35
	v_fmac_f32_e32 v229, v228, v68
	v_mul_f32_e32 v228, v231, v67
	v_fmac_f32_e32 v100, v230, v34
	v_fmac_f32_e32 v228, v230, v66
	v_add_f32_e32 v98, v98, v100
	v_add_f32_e32 v228, v229, v228
	v_add_f32_e32 v98, v97, v98
	v_add_f32_e32 v97, v99, v228
	s_waitcnt lgkmcnt(1)
	v_mul_f32_e32 v99, v225, v29
	v_mul_f32_e32 v225, v225, v61
	v_fmac_f32_e32 v99, v224, v28
	v_fmac_f32_e32 v225, v224, v60
	v_mul_f32_e32 v224, v227, v59
	v_fmac_f32_e32 v224, v226, v58
	v_mul_f32_e32 v100, v227, v27
	v_add_f32_e32 v224, v225, v224
	v_fmac_f32_e32 v100, v226, v26
	v_add_f32_e32 v97, v97, v224
	v_add_f32_e32 v99, v99, v100
	v_add_f32_e32 v98, v98, v99
	s_waitcnt lgkmcnt(0)
	v_mul_f32_e32 v99, v5, v25
	v_mul_f32_e32 v100, v7, v23
	v_fmac_f32_e32 v99, v4, v24
	v_fmac_f32_e32 v100, v6, v22
	v_add_f32_e32 v99, v99, v100
	v_add_f32_e32 v102, v98, v99
	ds_read_b128 v[236:239], v124
	ds_read_b128 v[232:235], v125
	ds_read_b128 v[228:231], v126
	ds_read_b128 v[224:227], v127
	ds_read_b128 v[98:101], v128
	ds_read_b128 v[240:243], v129
	v_mul_f32_e32 v5, v5, v57
	v_fmac_f32_e32 v5, v4, v56
	v_mul_f32_e32 v4, v7, v55
	v_fmac_f32_e32 v4, v6, v54
	v_add_f32_e32 v4, v5, v4
	v_add_f32_e32 v5, v97, v4
	s_waitcnt lgkmcnt(5)
	v_mul_f32_e32 v4, v237, v21
	v_mul_f32_e32 v6, v239, v19
	v_fmac_f32_e32 v4, v236, v20
	v_fmac_f32_e32 v6, v238, v18
	v_add_f32_e32 v4, v4, v6
	v_mul_f32_e32 v6, v237, v53
	v_mul_f32_e32 v7, v239, v51
	v_fmac_f32_e32 v6, v236, v52
	v_fmac_f32_e32 v7, v238, v50
	ds_read_b128 v[236:239], v130
	v_add_f32_e32 v6, v6, v7
	v_add_f32_e32 v5, v5, v6
	v_add_f32_e32 v4, v102, v4
	s_waitcnt lgkmcnt(5)
	v_mul_f32_e32 v6, v233, v49
	v_mul_f32_e32 v7, v235, v47
	v_fmac_f32_e32 v6, v232, v48
	v_fmac_f32_e32 v7, v234, v46
	v_add_f32_e32 v6, v6, v7
	v_mul_f32_e32 v7, v233, v73
	v_mul_f32_e32 v97, v235, v71
	v_fmac_f32_e32 v7, v232, v72
	v_fmac_f32_e32 v97, v234, v70
	ds_read_b128 v[232:235], v131
	v_add_f32_e32 v7, v7, v97
	v_add_f32_e32 v6, 0, v6
	v_add_f32_e32 v7, 0, v7
	s_waitcnt lgkmcnt(5)
	v_mul_f32_e32 v97, v229, v45
	v_mul_f32_e32 v102, v231, v43
	v_fmac_f32_e32 v97, v228, v44
	v_fmac_f32_e32 v102, v230, v42
	v_add_f32_e32 v97, v97, v102
	v_add_f32_e32 v6, v6, v97
	v_mul_f32_e32 v97, v229, v81
	v_fmac_f32_e32 v97, v228, v80
	v_mul_f32_e32 v228, v231, v79
	v_fmac_f32_e32 v228, v230, v78
	v_add_f32_e32 v97, v97, v228
	ds_read_b128 v[228:231], v132
	v_add_f32_e32 v7, v7, v97
	s_waitcnt lgkmcnt(5)
	v_mul_f32_e32 v97, v225, v41
	v_mul_f32_e32 v102, v227, v39
	v_fmac_f32_e32 v97, v224, v40
	v_fmac_f32_e32 v102, v226, v38
	v_add_f32_e32 v97, v97, v102
	v_add_f32_e32 v6, v6, v97
	v_mul_f32_e32 v97, v225, v77
	v_fmac_f32_e32 v97, v224, v76
	v_mul_f32_e32 v224, v227, v75
	v_fmac_f32_e32 v224, v226, v74
	v_add_f32_e32 v97, v97, v224
	ds_read_b128 v[224:227], v133
	v_add_f32_e32 v7, v7, v97
	s_waitcnt lgkmcnt(5)
	v_mul_f32_e32 v97, v99, v33
	v_mul_f32_e32 v102, v101, v31
	v_fmac_f32_e32 v97, v98, v32
	v_fmac_f32_e32 v102, v100, v30
	v_add_f32_e32 v97, v97, v102
	v_add_f32_e32 v6, v6, v97
	v_mul_f32_e32 v97, v99, v65
	v_fmac_f32_e32 v97, v98, v64
	v_mul_f32_e32 v98, v101, v63
	v_fmac_f32_e32 v98, v100, v62
	v_add_f32_e32 v97, v97, v98
	ds_read_b128 v[98:101], v134
	v_add_f32_e32 v7, v7, v97
	s_waitcnt lgkmcnt(5)
	v_mul_f32_e32 v97, v241, v37
	v_mul_f32_e32 v102, v243, v35
	v_fmac_f32_e32 v97, v240, v36
	v_fmac_f32_e32 v102, v242, v34
	v_add_f32_e32 v97, v97, v102
	v_add_f32_e32 v6, v6, v97
	v_mul_f32_e32 v97, v241, v69
	v_fmac_f32_e32 v97, v240, v68
	v_mul_f32_e32 v240, v243, v67
	v_fmac_f32_e32 v240, v242, v66
	v_add_f32_e32 v97, v97, v240
	ds_read_b128 v[240:243], v135
	v_add_f32_e32 v7, v7, v97
	s_waitcnt lgkmcnt(5)
	v_mul_f32_e32 v97, v237, v29
	v_mul_f32_e32 v102, v239, v27
	v_fmac_f32_e32 v97, v236, v28
	v_fmac_f32_e32 v102, v238, v26
	v_add_f32_e32 v97, v97, v102
	v_add_f32_e32 v6, v6, v97
	v_mul_f32_e32 v97, v237, v61
	v_fmac_f32_e32 v97, v236, v60
	v_mul_f32_e32 v236, v239, v59
	v_fmac_f32_e32 v236, v238, v58
	v_add_f32_e32 v97, v97, v236
	ds_read_b128 v[236:239], v136
	v_add_f32_e32 v7, v7, v97
	s_waitcnt lgkmcnt(5)
	v_mul_f32_e32 v97, v233, v25
	v_mul_f32_e32 v102, v235, v23
	v_fmac_f32_e32 v97, v232, v24
	v_fmac_f32_e32 v102, v234, v22
	v_add_f32_e32 v97, v97, v102
	v_add_f32_e32 v6, v6, v97
	v_mul_f32_e32 v97, v233, v57
	v_fmac_f32_e32 v97, v232, v56
	v_mul_f32_e32 v232, v235, v55
	v_fmac_f32_e32 v232, v234, v54
	v_add_f32_e32 v97, v97, v232
	ds_read_b128 v[232:235], v137
	v_add_f32_e32 v7, v7, v97
	s_waitcnt lgkmcnt(5)
	v_mul_f32_e32 v97, v229, v21
	v_mul_f32_e32 v102, v231, v19
	v_fmac_f32_e32 v97, v228, v20
	v_fmac_f32_e32 v102, v230, v18
	v_add_f32_e32 v97, v97, v102
	v_add_f32_e32 v6, v6, v97
	v_mul_f32_e32 v97, v229, v53
	v_fmac_f32_e32 v97, v228, v52
	v_mul_f32_e32 v228, v231, v51
	v_fmac_f32_e32 v228, v230, v50
	v_add_f32_e32 v97, v97, v228
	ds_read_b128 v[228:231], v138
	v_add_f32_e32 v7, v7, v97
	s_waitcnt lgkmcnt(5)
	v_mul_f32_e32 v97, v225, v49
	v_mul_f32_e32 v225, v225, v73
	v_fmac_f32_e32 v97, v224, v48
	v_fmac_f32_e32 v225, v224, v72
	v_mul_f32_e32 v224, v227, v71
	v_mul_f32_e32 v102, v227, v47
	v_fmac_f32_e32 v224, v226, v70
	v_fmac_f32_e32 v102, v226, v46
	v_add_f32_e32 v224, v225, v224
	v_add_f32_e32 v97, v97, v102
	v_add_f32_e32 v102, 0, v224
	ds_read_b128 v[224:227], v139
	v_add_f32_e32 v97, 0, v97
	s_waitcnt lgkmcnt(5)
	v_mul_f32_e32 v103, v99, v45
	v_mul_f32_e32 v99, v99, v81
	v_fmac_f32_e32 v103, v98, v44
	v_fmac_f32_e32 v99, v98, v80
	v_mul_f32_e32 v98, v101, v79
	v_fmac_f32_e32 v98, v100, v78
	v_mul_f32_e32 v104, v101, v43
	v_add_f32_e32 v98, v99, v98
	v_fmac_f32_e32 v104, v100, v42
	v_add_f32_e32 v102, v102, v98
	ds_read_b128 v[98:101], v140
	v_add_f32_e32 v103, v103, v104
	v_add_f32_e32 v97, v97, v103
	s_waitcnt lgkmcnt(5)
	v_mul_f32_e32 v103, v241, v41
	v_mul_f32_e32 v241, v241, v77
	v_fmac_f32_e32 v103, v240, v40
	v_fmac_f32_e32 v241, v240, v76
	v_mul_f32_e32 v240, v243, v75
	v_fmac_f32_e32 v240, v242, v74
	v_mul_f32_e32 v104, v243, v39
	v_add_f32_e32 v240, v241, v240
	v_fmac_f32_e32 v104, v242, v38
	v_add_f32_e32 v102, v102, v240
	v_add_f32_e32 v103, v103, v104
	v_add_f32_e32 v97, v97, v103
	s_waitcnt lgkmcnt(4)
	v_mul_f32_e32 v103, v237, v33
	v_mul_f32_e32 v237, v237, v65
	v_fmac_f32_e32 v103, v236, v32
	v_fmac_f32_e32 v237, v236, v64
	v_mul_f32_e32 v236, v239, v63
	v_fmac_f32_e32 v236, v238, v62
	v_mul_f32_e32 v104, v239, v31
	v_add_f32_e32 v236, v237, v236
	v_fmac_f32_e32 v104, v238, v30
	v_add_f32_e32 v102, v102, v236
	v_add_f32_e32 v103, v103, v104
	v_add_f32_e32 v97, v97, v103
	s_waitcnt lgkmcnt(3)
	v_mul_f32_e32 v103, v233, v37
	v_mul_f32_e32 v233, v233, v69
	v_fmac_f32_e32 v103, v232, v36
	v_fmac_f32_e32 v233, v232, v68
	v_mul_f32_e32 v232, v235, v67
	v_fmac_f32_e32 v232, v234, v66
	v_mul_f32_e32 v104, v235, v35
	v_add_f32_e32 v232, v233, v232
	v_fmac_f32_e32 v104, v234, v34
	v_add_f32_e32 v102, v102, v232
	v_add_f32_e32 v103, v103, v104
	v_add_f32_e32 v97, v97, v103
	s_waitcnt lgkmcnt(2)
	v_mul_f32_e32 v103, v229, v29
	v_mul_f32_e32 v229, v229, v61
	v_fmac_f32_e32 v103, v228, v28
	v_fmac_f32_e32 v229, v228, v60
	v_mul_f32_e32 v228, v231, v59
	v_fmac_f32_e32 v228, v230, v58
	v_mul_f32_e32 v104, v231, v27
	v_add_f32_e32 v228, v229, v228
	v_fmac_f32_e32 v104, v230, v26
	v_add_f32_e32 v102, v102, v228
	v_add_f32_e32 v103, v103, v104
	v_add_f32_e32 v97, v97, v103
	s_waitcnt lgkmcnt(1)
	v_mul_f32_e32 v103, v225, v25
	v_mul_f32_e32 v225, v225, v57
	v_fmac_f32_e32 v103, v224, v24
	v_fmac_f32_e32 v225, v224, v56
	v_mul_f32_e32 v224, v227, v55
	v_fmac_f32_e32 v224, v226, v54
	v_mul_f32_e32 v104, v227, v23
	v_add_f32_e32 v224, v225, v224
	v_fmac_f32_e32 v104, v226, v22
	v_add_f32_e32 v102, v102, v224
	v_add_f32_e32 v103, v103, v104
	v_add_f32_e32 v97, v97, v103
	s_waitcnt lgkmcnt(0)
	v_mul_f32_e32 v103, v99, v21
	v_mul_f32_e32 v99, v99, v53
	v_fmac_f32_e32 v103, v98, v20
	v_mul_f32_e32 v104, v101, v19
	v_fmac_f32_e32 v99, v98, v52
	v_mul_f32_e32 v98, v101, v51
	v_fmac_f32_e32 v104, v100, v18
	v_fmac_f32_e32 v98, v100, v50
	v_add_f32_e32 v103, v103, v104
	v_add_f32_e32 v98, v99, v98
	v_add_f32_e32 v97, v97, v103
	v_add_f32_e32 v98, v102, v98
	ds_read_b128 v[224:227], v141
	ds_read_b128 v[100:103], v142
	ds_read_b128 v[240:243], v143
	ds_read_b128 v[236:239], v144
	ds_read_b128 v[232:235], v145
	ds_read_b128 v[228:231], v146
	s_waitcnt lgkmcnt(5)
	v_mul_f32_e32 v99, v225, v49
	v_mul_f32_e32 v225, v225, v73
	v_fmac_f32_e32 v99, v224, v48
	v_fmac_f32_e32 v225, v224, v72
	v_mul_f32_e32 v224, v227, v71
	v_mul_f32_e32 v104, v227, v47
	v_fmac_f32_e32 v224, v226, v70
	v_fmac_f32_e32 v104, v226, v46
	v_add_f32_e32 v224, v225, v224
	v_add_f32_e32 v99, v99, v104
	v_add_f32_e32 v104, 0, v224
	ds_read_b128 v[224:227], v147
	v_add_f32_e32 v99, 0, v99
	s_waitcnt lgkmcnt(5)
	v_mul_f32_e32 v105, v101, v45
	v_mul_f32_e32 v101, v101, v81
	v_fmac_f32_e32 v105, v100, v44
	v_fmac_f32_e32 v101, v100, v80
	v_mul_f32_e32 v100, v103, v79
	v_fmac_f32_e32 v100, v102, v78
	v_mul_f32_e32 v106, v103, v43
	v_add_f32_e32 v100, v101, v100
	v_fmac_f32_e32 v106, v102, v42
	v_add_f32_e32 v104, v104, v100
	ds_read_b128 v[100:103], v148
	v_add_f32_e32 v105, v105, v106
	v_add_f32_e32 v99, v99, v105
	s_waitcnt lgkmcnt(5)
	v_mul_f32_e32 v105, v241, v41
	v_mul_f32_e32 v241, v241, v77
	v_fmac_f32_e32 v105, v240, v40
	v_fmac_f32_e32 v241, v240, v76
	v_mul_f32_e32 v240, v243, v75
	v_fmac_f32_e32 v240, v242, v74
	v_mul_f32_e32 v106, v243, v39
	v_add_f32_e32 v240, v241, v240
	v_fmac_f32_e32 v106, v242, v38
	v_add_f32_e32 v104, v104, v240
	v_add_f32_e32 v105, v105, v106
	v_add_f32_e32 v99, v99, v105
	s_waitcnt lgkmcnt(4)
	v_mul_f32_e32 v105, v237, v33
	v_mul_f32_e32 v237, v237, v65
	v_fmac_f32_e32 v105, v236, v32
	v_fmac_f32_e32 v237, v236, v64
	v_mul_f32_e32 v236, v239, v63
	v_fmac_f32_e32 v236, v238, v62
	v_mul_f32_e32 v106, v239, v31
	v_add_f32_e32 v236, v237, v236
	v_fmac_f32_e32 v106, v238, v30
	v_add_f32_e32 v104, v104, v236
	v_add_f32_e32 v105, v105, v106
	v_add_f32_e32 v99, v99, v105
	s_waitcnt lgkmcnt(3)
	v_mul_f32_e32 v105, v233, v37
	v_mul_f32_e32 v233, v233, v69
	v_fmac_f32_e32 v105, v232, v36
	v_fmac_f32_e32 v233, v232, v68
	v_mul_f32_e32 v232, v235, v67
	v_fmac_f32_e32 v232, v234, v66
	v_mul_f32_e32 v106, v235, v35
	v_add_f32_e32 v232, v233, v232
	v_fmac_f32_e32 v106, v234, v34
	v_add_f32_e32 v104, v104, v232
	v_add_f32_e32 v105, v105, v106
	v_add_f32_e32 v99, v99, v105
	s_waitcnt lgkmcnt(2)
	v_mul_f32_e32 v105, v229, v29
	v_mul_f32_e32 v229, v229, v61
	v_fmac_f32_e32 v105, v228, v28
	v_fmac_f32_e32 v229, v228, v60
	v_mul_f32_e32 v228, v231, v59
	v_fmac_f32_e32 v228, v230, v58
	v_mul_f32_e32 v106, v231, v27
	v_add_f32_e32 v228, v229, v228
	v_fmac_f32_e32 v106, v230, v26
	v_add_f32_e32 v104, v104, v228
	v_add_f32_e32 v105, v105, v106
	v_add_f32_e32 v99, v99, v105
	s_waitcnt lgkmcnt(1)
	v_mul_f32_e32 v105, v225, v25
	v_mul_f32_e32 v225, v225, v57
	v_fmac_f32_e32 v105, v224, v24
	v_fmac_f32_e32 v225, v224, v56
	v_mul_f32_e32 v224, v227, v55
	v_fmac_f32_e32 v224, v226, v54
	v_mul_f32_e32 v106, v227, v23
	v_add_f32_e32 v224, v225, v224
	v_fmac_f32_e32 v106, v226, v22
	v_add_f32_e32 v104, v104, v224
	v_add_f32_e32 v105, v105, v106
	v_add_f32_e32 v99, v99, v105
	s_waitcnt lgkmcnt(0)
	v_mul_f32_e32 v105, v101, v21
	v_mul_f32_e32 v101, v101, v53
	v_fmac_f32_e32 v105, v100, v20
	v_mul_f32_e32 v106, v103, v19
	v_fmac_f32_e32 v101, v100, v52
	v_mul_f32_e32 v100, v103, v51
	v_fmac_f32_e32 v106, v102, v18
	v_fmac_f32_e32 v100, v102, v50
	v_add_f32_e32 v105, v105, v106
	v_add_f32_e32 v100, v101, v100
	v_add_f32_e32 v99, v99, v105
	v_add_f32_e32 v100, v104, v100
	ds_read_b128 v[224:227], v149
	ds_read_b128 v[102:105], v150
	ds_read_b128 v[240:243], v151
	ds_read_b128 v[236:239], v152
	ds_read_b128 v[232:235], v153
	ds_read_b128 v[228:231], v154
	s_waitcnt lgkmcnt(5)
	v_mul_f32_e32 v101, v225, v49
	v_mul_f32_e32 v225, v225, v73
	v_fmac_f32_e32 v101, v224, v48
	v_fmac_f32_e32 v225, v224, v72
	v_mul_f32_e32 v224, v227, v71
	v_mul_f32_e32 v106, v227, v47
	v_fmac_f32_e32 v224, v226, v70
	v_fmac_f32_e32 v106, v226, v46
	v_add_f32_e32 v224, v225, v224
	v_add_f32_e32 v101, v101, v106
	v_add_f32_e32 v106, 0, v224
	ds_read_b128 v[224:227], v155
	v_add_f32_e32 v101, 0, v101
	s_waitcnt lgkmcnt(5)
	v_mul_f32_e32 v107, v103, v45
	v_mul_f32_e32 v103, v103, v81
	v_fmac_f32_e32 v107, v102, v44
	v_fmac_f32_e32 v103, v102, v80
	v_mul_f32_e32 v102, v105, v79
	v_fmac_f32_e32 v102, v104, v78
	v_mul_f32_e32 v108, v105, v43
	v_add_f32_e32 v102, v103, v102
	v_fmac_f32_e32 v108, v104, v42
	v_add_f32_e32 v106, v106, v102
	ds_read_b128 v[102:105], v156
	v_add_f32_e32 v107, v107, v108
	v_add_f32_e32 v101, v101, v107
	s_waitcnt lgkmcnt(5)
	v_mul_f32_e32 v107, v241, v41
	v_mul_f32_e32 v241, v241, v77
	v_fmac_f32_e32 v107, v240, v40
	v_fmac_f32_e32 v241, v240, v76
	v_mul_f32_e32 v240, v243, v75
	v_fmac_f32_e32 v240, v242, v74
	v_mul_f32_e32 v108, v243, v39
	v_add_f32_e32 v240, v241, v240
	v_fmac_f32_e32 v108, v242, v38
	v_add_f32_e32 v106, v106, v240
	v_add_f32_e32 v107, v107, v108
	v_add_f32_e32 v101, v101, v107
	s_waitcnt lgkmcnt(4)
	v_mul_f32_e32 v107, v237, v33
	v_mul_f32_e32 v237, v237, v65
	v_fmac_f32_e32 v107, v236, v32
	v_fmac_f32_e32 v237, v236, v64
	v_mul_f32_e32 v236, v239, v63
	v_fmac_f32_e32 v236, v238, v62
	v_mul_f32_e32 v108, v239, v31
	v_add_f32_e32 v236, v237, v236
	v_fmac_f32_e32 v108, v238, v30
	v_add_f32_e32 v106, v106, v236
	v_add_f32_e32 v107, v107, v108
	v_add_f32_e32 v101, v101, v107
	s_waitcnt lgkmcnt(3)
	v_mul_f32_e32 v107, v233, v37
	v_mul_f32_e32 v233, v233, v69
	v_fmac_f32_e32 v107, v232, v36
	v_fmac_f32_e32 v233, v232, v68
	v_mul_f32_e32 v232, v235, v67
	v_fmac_f32_e32 v232, v234, v66
	v_mul_f32_e32 v108, v235, v35
	v_add_f32_e32 v232, v233, v232
	v_fmac_f32_e32 v108, v234, v34
	v_add_f32_e32 v106, v106, v232
	v_add_f32_e32 v107, v107, v108
	v_add_f32_e32 v101, v101, v107
	s_waitcnt lgkmcnt(2)
	v_mul_f32_e32 v107, v229, v29
	v_mul_f32_e32 v229, v229, v61
	v_fmac_f32_e32 v107, v228, v28
	v_fmac_f32_e32 v229, v228, v60
	v_mul_f32_e32 v228, v231, v59
	v_fmac_f32_e32 v228, v230, v58
	v_mul_f32_e32 v108, v231, v27
	v_add_f32_e32 v228, v229, v228
	v_fmac_f32_e32 v108, v230, v26
	v_add_f32_e32 v106, v106, v228
	v_add_f32_e32 v107, v107, v108
	v_add_f32_e32 v101, v101, v107
	s_waitcnt lgkmcnt(1)
	v_mul_f32_e32 v107, v225, v25
	v_mul_f32_e32 v225, v225, v57
	v_fmac_f32_e32 v107, v224, v24
	v_fmac_f32_e32 v225, v224, v56
	v_mul_f32_e32 v224, v227, v55
	v_fmac_f32_e32 v224, v226, v54
	v_mul_f32_e32 v108, v227, v23
	v_add_f32_e32 v224, v225, v224
	v_fmac_f32_e32 v108, v226, v22
	v_add_f32_e32 v106, v106, v224
	v_add_f32_e32 v107, v107, v108
	v_add_f32_e32 v101, v101, v107
	s_waitcnt lgkmcnt(0)
	v_mul_f32_e32 v107, v103, v21
	v_mul_f32_e32 v103, v103, v53
	v_fmac_f32_e32 v107, v102, v20
	v_mul_f32_e32 v108, v105, v19
	v_fmac_f32_e32 v103, v102, v52
	v_mul_f32_e32 v102, v105, v51
	v_fmac_f32_e32 v108, v104, v18
	v_fmac_f32_e32 v102, v104, v50
	v_add_f32_e32 v107, v107, v108
	v_add_f32_e32 v102, v103, v102
	v_add_f32_e32 v101, v101, v107
	v_add_f32_e32 v102, v106, v102
	ds_read_b128 v[224:227], v157
	ds_read_b128 v[104:107], v158
	ds_read_b128 v[240:243], v159
	ds_read_b128 v[236:239], v160
	ds_read_b128 v[232:235], v161
	ds_read_b128 v[228:231], v162
	s_waitcnt lgkmcnt(5)
	v_mul_f32_e32 v103, v225, v49
	v_mul_f32_e32 v225, v225, v73
	v_fmac_f32_e32 v103, v224, v48
	v_fmac_f32_e32 v225, v224, v72
	v_mul_f32_e32 v224, v227, v71
	v_mul_f32_e32 v108, v227, v47
	v_fmac_f32_e32 v224, v226, v70
	v_fmac_f32_e32 v108, v226, v46
	v_add_f32_e32 v224, v225, v224
	v_add_f32_e32 v103, v103, v108
	v_add_f32_e32 v108, 0, v224
	ds_read_b128 v[224:227], v163
	v_add_f32_e32 v103, 0, v103
	s_waitcnt lgkmcnt(5)
	v_mul_f32_e32 v109, v105, v45
	v_mul_f32_e32 v105, v105, v81
	v_fmac_f32_e32 v109, v104, v44
	v_fmac_f32_e32 v105, v104, v80
	v_mul_f32_e32 v104, v107, v79
	v_fmac_f32_e32 v104, v106, v78
	v_mul_f32_e32 v191, v107, v43
	v_add_f32_e32 v104, v105, v104
	v_fmac_f32_e32 v191, v106, v42
	v_add_f32_e32 v108, v108, v104
	ds_read_b128 v[104:107], v164
	v_add_f32_e32 v109, v109, v191
	v_add_f32_e32 v103, v103, v109
	s_waitcnt lgkmcnt(5)
	v_mul_f32_e32 v109, v241, v41
	v_mul_f32_e32 v241, v241, v77
	v_fmac_f32_e32 v109, v240, v40
	v_fmac_f32_e32 v241, v240, v76
	v_mul_f32_e32 v240, v243, v75
	v_fmac_f32_e32 v240, v242, v74
	v_mul_f32_e32 v191, v243, v39
	v_add_f32_e32 v240, v241, v240
	v_fmac_f32_e32 v191, v242, v38
	v_add_f32_e32 v108, v108, v240
	v_add_f32_e32 v109, v109, v191
	v_add_f32_e32 v103, v103, v109
	s_waitcnt lgkmcnt(4)
	v_mul_f32_e32 v109, v237, v33
	v_mul_f32_e32 v237, v237, v65
	v_fmac_f32_e32 v109, v236, v32
	v_fmac_f32_e32 v237, v236, v64
	v_mul_f32_e32 v236, v239, v63
	v_fmac_f32_e32 v236, v238, v62
	v_mul_f32_e32 v191, v239, v31
	v_add_f32_e32 v236, v237, v236
	v_fmac_f32_e32 v191, v238, v30
	v_add_f32_e32 v108, v108, v236
	v_add_f32_e32 v109, v109, v191
	v_add_f32_e32 v103, v103, v109
	s_waitcnt lgkmcnt(3)
	v_mul_f32_e32 v109, v233, v37
	v_mul_f32_e32 v233, v233, v69
	v_fmac_f32_e32 v109, v232, v36
	v_fmac_f32_e32 v233, v232, v68
	v_mul_f32_e32 v232, v235, v67
	v_fmac_f32_e32 v232, v234, v66
	v_mul_f32_e32 v191, v235, v35
	v_add_f32_e32 v232, v233, v232
	v_fmac_f32_e32 v191, v234, v34
	v_add_f32_e32 v108, v108, v232
	v_add_f32_e32 v109, v109, v191
	v_add_f32_e32 v103, v103, v109
	s_waitcnt lgkmcnt(2)
	v_mul_f32_e32 v109, v229, v29
	v_mul_f32_e32 v229, v229, v61
	v_fmac_f32_e32 v109, v228, v28
	v_fmac_f32_e32 v229, v228, v60
	v_mul_f32_e32 v228, v231, v59
	v_fmac_f32_e32 v228, v230, v58
	v_mul_f32_e32 v191, v231, v27
	v_add_f32_e32 v228, v229, v228
	v_fmac_f32_e32 v191, v230, v26
	v_add_f32_e32 v108, v108, v228
	v_add_f32_e32 v109, v109, v191
	v_add_f32_e32 v103, v103, v109
	s_waitcnt lgkmcnt(1)
	v_mul_f32_e32 v109, v225, v25
	v_mul_f32_e32 v225, v225, v57
	v_fmac_f32_e32 v109, v224, v24
	v_fmac_f32_e32 v225, v224, v56
	v_mul_f32_e32 v224, v227, v55
	v_fmac_f32_e32 v224, v226, v54
	v_mul_f32_e32 v191, v227, v23
	v_add_f32_e32 v224, v225, v224
	v_fmac_f32_e32 v191, v226, v22
	v_add_f32_e32 v108, v108, v224
	v_add_f32_e32 v109, v109, v191
	v_add_f32_e32 v103, v103, v109
	s_waitcnt lgkmcnt(0)
	v_mul_f32_e32 v109, v105, v21
	v_mul_f32_e32 v105, v105, v53
	v_fmac_f32_e32 v109, v104, v20
	v_mul_f32_e32 v191, v107, v19
	v_fmac_f32_e32 v105, v104, v52
	v_mul_f32_e32 v104, v107, v51
	v_fmac_f32_e32 v191, v106, v18
	v_fmac_f32_e32 v104, v106, v50
	v_add_f32_e32 v109, v109, v191
	v_add_f32_e32 v104, v105, v104
	v_add_f32_e32 v103, v103, v109
	v_add_f32_e32 v104, v108, v104
	ds_read_b128 v[224:227], v165
	ds_read_b128 v[106:109], v166
	ds_read_b128 v[240:243], v167
	ds_read_b128 v[236:239], v168
	ds_read_b128 v[232:235], v169
	ds_read_b128 v[228:231], v170
	s_waitcnt lgkmcnt(5)
	v_mul_f32_e32 v105, v225, v49
	v_mul_f32_e32 v225, v225, v73
	v_fmac_f32_e32 v105, v224, v48
	v_fmac_f32_e32 v225, v224, v72
	v_mul_f32_e32 v224, v227, v71
	v_mul_f32_e32 v191, v227, v47
	v_fmac_f32_e32 v224, v226, v70
	v_fmac_f32_e32 v191, v226, v46
	v_add_f32_e32 v224, v225, v224
	v_add_f32_e32 v105, v105, v191
	v_add_f32_e32 v191, 0, v224
	ds_read_b128 v[224:227], v171
	v_add_f32_e32 v105, 0, v105
	s_waitcnt lgkmcnt(5)
	v_mul_f32_e32 v192, v107, v45
	v_mul_f32_e32 v107, v107, v81
	v_fmac_f32_e32 v192, v106, v44
	v_fmac_f32_e32 v107, v106, v80
	v_mul_f32_e32 v106, v109, v79
	v_fmac_f32_e32 v106, v108, v78
	v_mul_f32_e32 v193, v109, v43
	v_add_f32_e32 v106, v107, v106
	v_fmac_f32_e32 v193, v108, v42
	v_add_f32_e32 v191, v191, v106
	ds_read_b128 v[106:109], v172
	v_add_f32_e32 v192, v192, v193
	v_add_f32_e32 v105, v105, v192
	s_waitcnt lgkmcnt(5)
	v_mul_f32_e32 v192, v241, v41
	v_mul_f32_e32 v241, v241, v77
	v_fmac_f32_e32 v192, v240, v40
	v_fmac_f32_e32 v241, v240, v76
	v_mul_f32_e32 v240, v243, v75
	v_fmac_f32_e32 v240, v242, v74
	v_mul_f32_e32 v193, v243, v39
	v_add_f32_e32 v240, v241, v240
	v_fmac_f32_e32 v193, v242, v38
	v_add_f32_e32 v191, v191, v240
	v_add_f32_e32 v192, v192, v193
	v_add_f32_e32 v105, v105, v192
	s_waitcnt lgkmcnt(4)
	v_mul_f32_e32 v192, v237, v33
	v_mul_f32_e32 v237, v237, v65
	v_fmac_f32_e32 v192, v236, v32
	v_fmac_f32_e32 v237, v236, v64
	v_mul_f32_e32 v236, v239, v63
	v_fmac_f32_e32 v236, v238, v62
	v_mul_f32_e32 v193, v239, v31
	v_add_f32_e32 v236, v237, v236
	v_fmac_f32_e32 v193, v238, v30
	v_add_f32_e32 v191, v191, v236
	v_add_f32_e32 v192, v192, v193
	v_add_f32_e32 v105, v105, v192
	s_waitcnt lgkmcnt(3)
	v_mul_f32_e32 v192, v233, v37
	v_mul_f32_e32 v233, v233, v69
	v_fmac_f32_e32 v192, v232, v36
	v_fmac_f32_e32 v233, v232, v68
	v_mul_f32_e32 v232, v235, v67
	v_fmac_f32_e32 v232, v234, v66
	v_mul_f32_e32 v193, v235, v35
	v_add_f32_e32 v232, v233, v232
	v_fmac_f32_e32 v193, v234, v34
	v_add_f32_e32 v191, v191, v232
	v_add_f32_e32 v192, v192, v193
	v_add_f32_e32 v105, v105, v192
	s_waitcnt lgkmcnt(2)
	v_mul_f32_e32 v192, v229, v29
	v_mul_f32_e32 v229, v229, v61
	v_fmac_f32_e32 v192, v228, v28
	v_fmac_f32_e32 v229, v228, v60
	v_mul_f32_e32 v228, v231, v59
	v_fmac_f32_e32 v228, v230, v58
	v_mul_f32_e32 v193, v231, v27
	v_add_f32_e32 v228, v229, v228
	v_fmac_f32_e32 v193, v230, v26
	v_add_f32_e32 v191, v191, v228
	v_add_f32_e32 v192, v192, v193
	v_add_f32_e32 v105, v105, v192
	s_waitcnt lgkmcnt(1)
	v_mul_f32_e32 v192, v225, v25
	v_mul_f32_e32 v225, v225, v57
	v_fmac_f32_e32 v192, v224, v24
	v_fmac_f32_e32 v225, v224, v56
	v_mul_f32_e32 v224, v227, v55
	v_fmac_f32_e32 v224, v226, v54
	v_mul_f32_e32 v193, v227, v23
	v_add_f32_e32 v224, v225, v224
	v_fmac_f32_e32 v193, v226, v22
	v_add_f32_e32 v191, v191, v224
	v_add_f32_e32 v192, v192, v193
	v_add_f32_e32 v105, v105, v192
	s_waitcnt lgkmcnt(0)
	v_mul_f32_e32 v192, v107, v21
	v_mul_f32_e32 v193, v109, v19
	v_fmac_f32_e32 v192, v106, v20
	v_fmac_f32_e32 v193, v108, v18
	v_add_f32_e32 v192, v192, v193
	v_add_f32_e32 v105, v105, v192
	ds_read_b128 v[192:195], v173
	v_mul_f32_e32 v107, v107, v53
	v_fmac_f32_e32 v107, v106, v52
	v_mul_f32_e32 v106, v109, v51
	v_fmac_f32_e32 v106, v108, v50
	s_waitcnt lgkmcnt(0)
	v_mul_f32_e32 v49, v193, v49
	v_mul_f32_e32 v47, v195, v47
	v_fmac_f32_e32 v49, v192, v48
	v_fmac_f32_e32 v47, v194, v46
	v_add_f32_e32 v46, v49, v47
	v_add_f32_e32 v106, v107, v106
	v_add_f32_e32 v107, 0, v46
	v_mul_f32_e32 v46, v193, v73
	v_mul_f32_e32 v47, v195, v71
	v_fmac_f32_e32 v46, v192, v72
	v_fmac_f32_e32 v47, v194, v70
	v_add_f32_e32 v46, v46, v47
	v_add_f32_e32 v70, 0, v46
	ds_read_b128 v[46:49], v174
	v_add_f32_e32 v106, v191, v106
	s_waitcnt lgkmcnt(0)
	v_mul_f32_e32 v45, v47, v45
	v_mul_f32_e32 v43, v49, v43
	v_fmac_f32_e32 v45, v46, v44
	v_fmac_f32_e32 v43, v48, v42
	v_add_f32_e32 v42, v45, v43
	v_add_f32_e32 v71, v107, v42
	v_mul_f32_e32 v42, v47, v81
	v_mul_f32_e32 v43, v49, v79
	v_fmac_f32_e32 v42, v46, v80
	v_fmac_f32_e32 v43, v48, v78
	v_add_f32_e32 v42, v42, v43
	v_add_f32_e32 v46, v70, v42
	ds_read_b128 v[42:45], v175
	s_waitcnt lgkmcnt(0)
	v_mul_f32_e32 v41, v43, v41
	v_mul_f32_e32 v39, v45, v39
	v_fmac_f32_e32 v41, v42, v40
	v_fmac_f32_e32 v39, v44, v38
	v_add_f32_e32 v38, v41, v39
	v_add_f32_e32 v47, v71, v38
	v_mul_f32_e32 v38, v43, v77
	v_mul_f32_e32 v39, v45, v75
	v_fmac_f32_e32 v38, v42, v76
	v_fmac_f32_e32 v39, v44, v74
	v_add_f32_e32 v38, v38, v39
	v_add_f32_e32 v42, v46, v38
	ds_read_b128 v[38:41], v176
	s_waitcnt lgkmcnt(0)
	v_mul_f32_e32 v33, v39, v33
	v_mul_f32_e32 v31, v41, v31
	v_fmac_f32_e32 v33, v38, v32
	v_fmac_f32_e32 v31, v40, v30
	v_add_f32_e32 v30, v33, v31
	v_add_f32_e32 v43, v47, v30
	v_mul_f32_e32 v30, v39, v65
	v_mul_f32_e32 v31, v41, v63
	v_fmac_f32_e32 v30, v38, v64
	v_fmac_f32_e32 v31, v40, v62
	v_add_f32_e32 v30, v30, v31
	v_add_f32_e32 v38, v42, v30
	ds_read_b128 v[224:227], v177
	ds_read_b128 v[30:33], v178
	s_waitcnt lgkmcnt(1)
	v_mul_f32_e32 v37, v225, v37
	v_mul_f32_e32 v225, v225, v69
	v_fmac_f32_e32 v37, v224, v36
	v_fmac_f32_e32 v225, v224, v68
	v_mul_f32_e32 v224, v227, v67
	v_mul_f32_e32 v35, v227, v35
	v_fmac_f32_e32 v224, v226, v66
	v_fmac_f32_e32 v35, v226, v34
	v_add_f32_e32 v224, v225, v224
	v_add_f32_e32 v34, v37, v35
	v_add_f32_e32 v35, v38, v224
	v_add_f32_e32 v34, v43, v34
	s_waitcnt lgkmcnt(0)
	v_mul_f32_e32 v29, v31, v29
	v_mul_f32_e32 v27, v33, v27
	v_fmac_f32_e32 v29, v30, v28
	v_fmac_f32_e32 v27, v32, v26
	v_add_f32_e32 v26, v29, v27
	v_add_f32_e32 v34, v34, v26
	v_mul_f32_e32 v26, v31, v61
	v_mul_f32_e32 v27, v33, v59
	v_fmac_f32_e32 v26, v30, v60
	v_fmac_f32_e32 v27, v32, v58
	v_add_f32_e32 v26, v26, v27
	v_add_f32_e32 v30, v35, v26
	ds_read_b128 v[26:29], v179
	s_waitcnt lgkmcnt(0)
	v_mul_f32_e32 v25, v27, v25
	v_mul_f32_e32 v23, v29, v23
	v_fmac_f32_e32 v25, v26, v24
	v_fmac_f32_e32 v23, v28, v22
	v_add_f32_e32 v22, v25, v23
	v_add_f32_e32 v31, v34, v22
	v_mul_f32_e32 v22, v27, v57
	v_mul_f32_e32 v23, v29, v55
	v_fmac_f32_e32 v22, v26, v56
	v_fmac_f32_e32 v23, v28, v54
	v_add_f32_e32 v22, v22, v23
	v_add_f32_e32 v26, v30, v22
	ds_read_b128 v[22:25], v180
	v_cndmask_b32_e64 v27, v92, v104, s[34:35]
	v_cndmask_b32_e64 v28, v104, v92, s[34:35]
	v_cndmask_b32_e64 v29, v94, v106, s[34:35]
	v_cndmask_b32_e64 v30, v106, v94, s[34:35]
	s_waitcnt lgkmcnt(0)
	v_mul_f32_e32 v21, v23, v21
	v_mul_f32_e32 v19, v25, v19
	v_fmac_f32_e32 v21, v22, v20
	v_fmac_f32_e32 v19, v24, v18
	v_add_f32_e32 v18, v21, v19
	v_mul_f32_e32 v19, v23, v53
	v_mul_f32_e32 v20, v25, v51
	v_fmac_f32_e32 v19, v22, v52
	v_fmac_f32_e32 v20, v24, v50
	v_add_f32_e32 v19, v19, v20
	v_cndmask_b32_e64 v20, v2, v4, s[34:35]
	v_cndmask_b32_e64 v2, v4, v2, s[34:35]
	v_cndmask_b32_e64 v4, v82, v5, s[34:35]
	ds_bpermute_b32 v4, v112, v4
	v_cndmask_b32_e64 v5, v5, v82, s[34:35]
	ds_bpermute_b32 v20, v112, v20
	v_cndmask_b32_e64 v21, v86, v98, s[34:35]
	v_cndmask_b32_e64 v22, v98, v86, s[34:35]
	s_waitcnt lgkmcnt(1)
	v_add_f32_e32 v4, v5, v4
	v_cndmask_b32_e64 v5, v83, v6, s[34:35]
	ds_bpermute_b32 v5, v112, v5
	s_waitcnt lgkmcnt(1)
	v_add_f32_e32 v2, v2, v20
	v_cndmask_b32_e64 v6, v6, v83, s[34:35]
	v_cndmask_b32_e64 v20, v84, v7, s[34:35]
	v_cndmask_b32_e64 v7, v7, v84, s[34:35]
	s_waitcnt lgkmcnt(0)
	v_add_f32_e32 v5, v6, v5
	ds_bpermute_b32 v6, v112, v20
	v_cndmask_b32_e64 v20, v97, v85, s[34:35]
	v_cndmask_b32_e64 v23, v88, v100, s[34:35]
	v_cndmask_b32_e64 v24, v100, v88, s[34:35]
	v_cndmask_b32_e64 v25, v90, v102, s[34:35]
	s_waitcnt lgkmcnt(0)
	v_add_f32_e32 v6, v7, v6
	v_cndmask_b32_e64 v7, v85, v97, s[34:35]
	ds_bpermute_b32 v7, v112, v7
	v_add_f32_e32 v19, v26, v19
	v_cndmask_b32_e64 v26, v102, v90, s[34:35]
	v_add_f32_e32 v18, v31, v18
	s_waitcnt lgkmcnt(0)
	v_add_f32_e32 v7, v20, v7
	ds_bpermute_b32 v20, v112, v21
	v_cndmask_b32_e64 v21, v87, v99, s[34:35]
	ds_bpermute_b32 v21, v112, v21
	s_waitcnt lgkmcnt(1)
	v_add_f32_e32 v20, v22, v20
	v_cndmask_b32_e64 v22, v99, v87, s[34:35]
	s_waitcnt lgkmcnt(0)
	v_add_f32_e32 v21, v22, v21
	ds_bpermute_b32 v22, v112, v23
	v_cndmask_b32_e64 v23, v89, v101, s[34:35]
	ds_bpermute_b32 v23, v112, v23
	s_waitcnt lgkmcnt(1)
	v_add_f32_e32 v22, v24, v22
	v_cndmask_b32_e64 v24, v101, v89, s[34:35]
	s_waitcnt lgkmcnt(0)
	v_add_f32_e32 v23, v24, v23
	ds_bpermute_b32 v24, v112, v25
	v_cndmask_b32_e64 v25, v91, v103, s[34:35]
	ds_bpermute_b32 v25, v112, v25
	s_waitcnt lgkmcnt(1)
	v_add_f32_e32 v24, v26, v24
	v_cndmask_b32_e64 v26, v103, v91, s[34:35]
	s_waitcnt lgkmcnt(0)
	v_add_f32_e32 v25, v26, v25
	ds_bpermute_b32 v26, v112, v27
	v_cndmask_b32_e64 v27, v93, v105, s[34:35]
	ds_bpermute_b32 v27, v112, v27
	s_waitcnt lgkmcnt(1)
	v_add_f32_e32 v26, v28, v26
	v_cndmask_b32_e64 v28, v105, v93, s[34:35]
	s_waitcnt lgkmcnt(0)
	v_add_f32_e32 v27, v28, v27
	ds_bpermute_b32 v28, v112, v29
	v_cndmask_b32_e64 v29, v95, v18, s[34:35]
	ds_bpermute_b32 v29, v112, v29
	v_cndmask_b32_e64 v18, v18, v95, s[34:35]
	s_waitcnt lgkmcnt(1)
	v_add_f32_e32 v28, v30, v28
	v_cndmask_b32_e64 v30, v96, v19, s[34:35]
	s_waitcnt lgkmcnt(0)
	v_add_f32_e32 v18, v18, v29
	ds_bpermute_b32 v29, v112, v30
	v_cndmask_b32_e64 v19, v19, v96, s[34:35]
	s_waitcnt lgkmcnt(0)
	v_add_f32_e32 v19, v19, v29
	v_cndmask_b32_e64 v29, v2, v23, s[36:37]
	v_cndmask_b32_e64 v2, v23, v2, s[36:37]
	v_cndmask_b32_e64 v23, v4, v24, s[36:37]
	ds_bpermute_b32 v23, v111, v23
	v_cndmask_b32_e64 v4, v24, v4, s[36:37]
	ds_bpermute_b32 v24, v111, v29
	s_waitcnt lgkmcnt(1)
	v_add_f32_e32 v4, v4, v23
	v_cndmask_b32_e64 v23, v5, v25, s[36:37]
	ds_bpermute_b32 v23, v111, v23
	s_waitcnt lgkmcnt(1)
	v_add_f32_e32 v2, v2, v24
	v_cndmask_b32_e64 v5, v25, v5, s[36:37]
	v_cndmask_b32_e64 v24, v6, v26, s[36:37]
	v_cndmask_b32_e64 v6, v26, v6, s[36:37]
	s_waitcnt lgkmcnt(0)
	v_add_f32_e32 v5, v5, v23
	ds_bpermute_b32 v23, v111, v24
	v_cndmask_b32_e64 v24, v20, v28, s[36:37]
	v_cndmask_b32_e64 v20, v28, v20, s[36:37]
	s_waitcnt lgkmcnt(0)
	v_add_f32_e32 v6, v6, v23
	v_cndmask_b32_e64 v23, v7, v27, s[36:37]
	ds_bpermute_b32 v23, v111, v23
	v_cndmask_b32_e64 v7, v27, v7, s[36:37]
	s_waitcnt lgkmcnt(0)
	v_add_f32_e32 v7, v7, v23
	ds_bpermute_b32 v23, v111, v24
	s_waitcnt lgkmcnt(0)
	v_add_f32_e32 v20, v20, v23
	v_cndmask_b32_e64 v23, v21, v18, s[36:37]
	v_cndmask_b32_e64 v18, v18, v21, s[36:37]
	v_cndmask_b32_e64 v21, v22, v19, s[36:37]
	ds_bpermute_b32 v21, v111, v21
	v_cndmask_b32_e64 v19, v19, v22, s[36:37]
	ds_bpermute_b32 v22, v111, v23
	s_waitcnt lgkmcnt(1)
	v_add_f32_e32 v19, v19, v21
	v_cndmask_b32_e64 v21, v2, v7, s[38:39]
	v_cndmask_b32_e64 v2, v7, v2, s[38:39]
	v_cndmask_b32_e64 v7, v4, v20, s[38:39]
	ds_bpermute_b32 v7, v113, v7
	s_waitcnt lgkmcnt(1)
	v_add_f32_e32 v18, v18, v22
	v_cndmask_b32_e64 v4, v20, v4, s[38:39]
	ds_bpermute_b32 v20, v113, v21
	s_waitcnt lgkmcnt(1)
	v_add_f32_e32 v4, v4, v7
	v_cndmask_b32_e64 v7, v5, v18, s[38:39]
	ds_bpermute_b32 v7, v113, v7
	v_cndmask_b32_e64 v5, v18, v5, s[38:39]
	v_cndmask_b32_e64 v18, v6, v19, s[38:39]
	s_waitcnt lgkmcnt(1)
	v_add_f32_e32 v2, v2, v20
	v_cndmask_b32_e64 v6, v19, v6, s[38:39]
	s_waitcnt lgkmcnt(0)
	v_add_f32_e32 v5, v5, v7
	ds_bpermute_b32 v7, v113, v18
	s_waitcnt lgkmcnt(0)
	v_add_f32_e32 v6, v6, v7
	v_cndmask_b32_e64 v7, v2, v5, s[40:41]
	v_cndmask_b32_e64 v2, v5, v2, s[40:41]
	v_cndmask_b32_e64 v5, v4, v6, s[40:41]
	v_cndmask_b32_e64 v4, v6, v4, s[40:41]
	ds_bpermute_b32 v6, v114, v7
	ds_bpermute_b32 v5, v114, v5
	s_waitcnt lgkmcnt(1)
	v_add_f32_e32 v2, v2, v6
	s_waitcnt lgkmcnt(0)
	v_add_f32_e32 v4, v4, v5
	ds_bpermute_b32 v5, v115, v2
	s_waitcnt lgkmcnt(0)
	v_add_f32_e32 v2, v2, v5
	ds_bpermute_b32 v5, v115, v4
	s_waitcnt lgkmcnt(0)
	v_add_f32_e32 v4, v4, v5
	ds_bpermute_b32 v5, v116, v2
	s_waitcnt lgkmcnt(0)
	v_add_f32_e32 v2, v2, v5
	ds_bpermute_b32 v5, v116, v4
	s_waitcnt lgkmcnt(0)
	v_add_f32_e32 v5, v4, v5
	ds_bpermute_b32 v4, v114, v2
	ds_bpermute_b32 v6, v114, v5
	s_waitcnt lgkmcnt(1)
	v_max_f32_e32 v4, v4, v4
	v_max_f32_e32 v4, v2, v4
	ds_bpermute_b32 v7, v113, v4
	s_waitcnt lgkmcnt(1)
	v_max_f32_e32 v6, v6, v6
	v_max_f32_e32 v6, v5, v6
	s_waitcnt lgkmcnt(0)
	v_max_f32_e32 v7, v7, v7
	v_max_f32_e32 v4, v4, v7
	ds_bpermute_b32 v7, v113, v6
	s_waitcnt lgkmcnt(0)
	v_max_f32_e32 v7, v7, v7
	v_max_f32_e32 v6, v6, v7
	ds_bpermute_b32 v7, v111, v4
	s_waitcnt lgkmcnt(0)
	v_max_f32_e32 v7, v7, v7
	v_max_f32_e32 v4, v4, v7
	ds_bpermute_b32 v7, v111, v6
	s_waitcnt lgkmcnt(0)
	v_max_f32_e32 v7, v7, v7
	v_max_f32_e32 v6, v6, v7
	ds_bpermute_b32 v7, v112, v4
	s_waitcnt lgkmcnt(0)
	v_max_f32_e32 v7, v7, v7
	v_max_f32_e32 v4, v4, v7
	ds_bpermute_b32 v7, v112, v6
	v_sub_f32_e32 v2, v2, v4
	v_mul_f32_e32 v2, 0x3fb8aa3b, v2
	v_exp_f32_e32 v4, v2
	s_waitcnt lgkmcnt(0)
	v_max_f32_e32 v7, v7, v7
	v_max_f32_e32 v6, v6, v7
	v_sub_f32_e32 v2, v5, v6
	v_mul_f32_e32 v2, 0x3fb8aa3b, v2
	ds_bpermute_b32 v5, v114, v4
	v_exp_f32_e32 v2, v2
	s_waitcnt lgkmcnt(0)
	v_add_f32_e32 v5, v4, v5
	ds_bpermute_b32 v6, v114, v2
	ds_bpermute_b32 v7, v113, v5
	s_waitcnt lgkmcnt(1)
	v_add_f32_e32 v6, v2, v6
	s_waitcnt lgkmcnt(0)
	v_add_f32_e32 v5, v5, v7
	ds_bpermute_b32 v7, v113, v6
	s_waitcnt lgkmcnt(0)
	v_add_f32_e32 v6, v6, v7
	ds_bpermute_b32 v7, v111, v5
	s_waitcnt lgkmcnt(0)
	v_add_f32_e32 v7, v5, v7
	ds_bpermute_b32 v5, v111, v6
	ds_bpermute_b32 v18, v112, v7
	s_waitcnt lgkmcnt(1)
	v_add_f32_e32 v5, v6, v5
	ds_bpermute_b32 v6, v112, v5
	s_and_saveexec_b64 s[0:1], s[42:43]
	s_cbranch_execz .LBB0_2122
	s_waitcnt lgkmcnt(1)
	v_add_f32_e32 v7, v7, v18
	v_div_scale_f32 v18, s[2:3], v7, v7, v4
	v_rcp_f32_e32 v19, v18
	v_div_scale_f32 v20, vcc, v4, v7, v4
	s_cmp_eq_u32 s8, s48
	v_fma_f32 v21, -v18, v19, 1.0
	v_fmac_f32_e32 v19, v21, v19
	v_mul_f32_e32 v21, v20, v19
	v_fma_f32 v22, -v18, v21, v20
	v_fmac_f32_e32 v21, v22, v19
	v_fma_f32 v18, -v18, v21, v20
	v_div_fmas_f32 v18, v18, v19, v21
	v_div_fixup_f32 v4, v18, v7, v4
	v_lshl_add_u64 v[18:19], s[44:45], 0, v[14:15]
	global_store_dword v[18:19], v4, off
	s_cbranch_scc1 .LBB0_2122
	s_waitcnt lgkmcnt(0)
	v_add_f32_e32 v4, v5, v6
	v_div_scale_f32 v5, s[2:3], v4, v4, v2
	v_rcp_f32_e32 v6, v5
	v_div_scale_f32 v7, vcc, v2, v4, v2
	s_lshl_b64 s[2:3], s[48:49], 6
	v_fma_f32 v18, -v5, v6, 1.0
	v_fmac_f32_e32 v6, v18, v6
	v_mul_f32_e32 v18, v7, v6
	v_fma_f32 v19, -v5, v18, v7
	v_fmac_f32_e32 v18, v19, v6
	v_fma_f32 v5, -v5, v18, v7
	v_div_fmas_f32 v5, v5, v6, v18
	v_div_fixup_f32 v2, v5, v4, v2
	v_lshl_add_u64 v[4:5], v[10:11], 0, s[2:3]
	global_store_dword v[4:5], v2, off
	s_branch .LBB0_2122
